# paired A windows: adjacent 512-B halves of each row requested back to back (4 stages, 4-buffer LDS ring), on top of v26
# speedup vs baseline: 1.0525x; 1.0512x over previous
.LBB1_235:
	v_mov_b32_e32 v110, v18
	v_mov_b32_e32 v111, v19
	v_mov_b32_e32 v112, v20
	v_mov_b32_e32 v113, v21
	s_mov_b32 s72, 0x2000
	s_mov_b32 s73, 0
	s_mov_b32 s74, 0x20000
	s_mov_b32 s75, 0
	v_lshl_add_u64 v[158:159], v[158:159], 0, s[74:75]
	v_mul_u32_u24_e32 v163, 0x110, v160
	v_lshl_add_u32 v162, v1, 4, v163
	global_load_dwordx4 v[94:97], v[158:159], off
	v_lshl_add_u64 v[158:159], v[158:159], 0, s[72:73]
	global_load_dwordx4 v[98:101], v[158:159], off
	v_lshl_add_u64 v[158:159], v[158:159], 0, s[72:73]
	global_load_dwordx4 v[102:105], v[158:159], off
	v_lshl_add_u64 v[158:159], v[158:159], 0, s[72:73]
	global_load_dwordx4 v[106:109], v[158:159], off
	v_lshl_add_u64 v[158:159], v[158:159], 0, s[72:73]
	global_load_dwordx4 v[142:145], v[158:159], off
	v_lshl_add_u64 v[158:159], v[158:159], 0, s[72:73]
	global_load_dwordx4 v[146:149], v[158:159], off
	v_lshl_add_u64 v[158:159], v[158:159], 0, s[72:73]
	global_load_dwordx4 v[150:153], v[158:159], off
	v_lshl_add_u64 v[158:159], v[158:159], 0, s[72:73]
	global_load_dwordx4 v[154:157], v[158:159], off
	v_lshl_add_u64 v[158:159], v[158:159], 0, s[72:73]
	s_waitcnt lgkmcnt(0)
	s_barrier
	ds_read_b128 v[114:117], v162 offset:0
	ds_read_b128 v[118:121], v162 offset:8704
	ds_read_b128 v[122:125], v162 offset:32
	ds_read_b128 v[126:129], v162 offset:8736
	ds_read_b128 v[130:133], v162 offset:64
	ds_read_b128 v[134:137], v162 offset:8768
	s_waitcnt lgkmcnt(5)
	v_mfma_f32_32x32x16_f16 v[2:17], v[114:117], v[110:113], 0
	s_waitcnt lgkmcnt(4)
	v_mfma_f32_32x32x16_f16 v[18:33], v[118:121], v[110:113], 0
	ds_read_b128 v[114:117], v162 offset:96
	ds_read_b128 v[118:121], v162 offset:8800
	global_load_dwordx4 v[110:113], v[158:159], off
	v_lshl_add_u64 v[158:159], v[158:159], 0, s[72:73]
	s_waitcnt lgkmcnt(5)
	v_mfma_f32_32x32x16_f16 v[2:17], v[122:125], v[90:93], v[2:17]
	s_waitcnt lgkmcnt(4)
	v_mfma_f32_32x32x16_f16 v[18:33], v[126:129], v[90:93], v[18:33]
	ds_read_b128 v[122:125], v162 offset:128
	ds_read_b128 v[126:129], v162 offset:8832
	global_load_dwordx4 v[90:93], v[158:159], off
	v_lshl_add_u64 v[158:159], v[158:159], 0, s[72:73]
	s_waitcnt lgkmcnt(5)
	v_mfma_f32_32x32x16_f16 v[2:17], v[130:133], v[86:89], v[2:17]
	s_waitcnt lgkmcnt(4)
	v_mfma_f32_32x32x16_f16 v[18:33], v[134:137], v[86:89], v[18:33]
	ds_read_b128 v[130:133], v162 offset:160
	ds_read_b128 v[134:137], v162 offset:8864
	global_load_dwordx4 v[86:89], v[158:159], off
	v_lshl_add_u64 v[158:159], v[158:159], 0, s[72:73]
	s_waitcnt lgkmcnt(5)
	v_mfma_f32_32x32x16_f16 v[2:17], v[114:117], v[82:85], v[2:17]
	s_waitcnt lgkmcnt(4)
	v_mfma_f32_32x32x16_f16 v[18:33], v[118:121], v[82:85], v[18:33]
	ds_read_b128 v[114:117], v162 offset:192
	ds_read_b128 v[118:121], v162 offset:8896
	global_load_dwordx4 v[82:85], v[158:159], off
	v_lshl_add_u64 v[158:159], v[158:159], 0, s[72:73]
	s_waitcnt lgkmcnt(5)
	v_mfma_f32_32x32x16_f16 v[2:17], v[122:125], v[78:81], v[2:17]
	s_waitcnt lgkmcnt(4)
	v_mfma_f32_32x32x16_f16 v[18:33], v[126:129], v[78:81], v[18:33]
	ds_read_b128 v[122:125], v162 offset:224
	ds_read_b128 v[126:129], v162 offset:8928
	global_load_dwordx4 v[78:81], v[158:159], off
	v_lshl_add_u64 v[158:159], v[158:159], 0, s[72:73]
	s_waitcnt lgkmcnt(5)
	v_mfma_f32_32x32x16_f16 v[2:17], v[130:133], v[74:77], v[2:17]
	s_waitcnt lgkmcnt(4)
	v_mfma_f32_32x32x16_f16 v[18:33], v[134:137], v[74:77], v[18:33]
	global_load_dwordx4 v[74:77], v[158:159], off
	v_lshl_add_u64 v[158:159], v[158:159], 0, s[72:73]
	s_waitcnt lgkmcnt(3)
	v_mfma_f32_32x32x16_f16 v[2:17], v[114:117], v[70:73], v[2:17]
	s_waitcnt lgkmcnt(2)
	v_mfma_f32_32x32x16_f16 v[18:33], v[118:121], v[70:73], v[18:33]
	global_load_dwordx4 v[70:73], v[158:159], off
	v_lshl_add_u64 v[158:159], v[158:159], 0, s[72:73]
	s_waitcnt lgkmcnt(1)
	v_mfma_f32_32x32x16_f16 v[2:17], v[122:125], v[66:69], v[2:17]
	s_waitcnt lgkmcnt(0)
	v_mfma_f32_32x32x16_f16 v[18:33], v[126:129], v[66:69], v[18:33]
	global_load_dwordx4 v[66:69], v[158:159], off
	v_lshl_add_u64 v[158:159], v[158:159], 0, s[72:73]
	s_waitcnt lgkmcnt(0)
	s_barrier
	ds_read_b128 v[114:117], v162 offset:17408
	ds_read_b128 v[118:121], v162 offset:26112
	ds_read_b128 v[122:125], v162 offset:17440
	ds_read_b128 v[126:129], v162 offset:26144
	ds_read_b128 v[130:133], v162 offset:17472
	ds_read_b128 v[134:137], v162 offset:26176
	s_waitcnt lgkmcnt(5)
	v_mfma_f32_32x32x16_f16 v[2:17], v[114:117], v[62:65], v[2:17]
	s_waitcnt lgkmcnt(4)
	v_mfma_f32_32x32x16_f16 v[18:33], v[118:121], v[62:65], v[18:33]
	ds_read_b128 v[114:117], v162 offset:17504
	ds_read_b128 v[118:121], v162 offset:26208
	global_load_dwordx4 v[62:65], v[158:159], off
	v_lshl_add_u64 v[158:159], v[158:159], 0, s[72:73]
	s_waitcnt lgkmcnt(5)
	v_mfma_f32_32x32x16_f16 v[2:17], v[122:125], v[58:61], v[2:17]
	s_waitcnt lgkmcnt(4)
	v_mfma_f32_32x32x16_f16 v[18:33], v[126:129], v[58:61], v[18:33]
	ds_read_b128 v[122:125], v162 offset:17536
	ds_read_b128 v[126:129], v162 offset:26240
	global_load_dwordx4 v[58:61], v[158:159], off
	v_lshl_add_u64 v[158:159], v[158:159], 0, s[72:73]
	s_waitcnt lgkmcnt(5)
	v_mfma_f32_32x32x16_f16 v[2:17], v[130:133], v[54:57], v[2:17]
	s_waitcnt lgkmcnt(4)
	v_mfma_f32_32x32x16_f16 v[18:33], v[134:137], v[54:57], v[18:33]
	ds_read_b128 v[130:133], v162 offset:17568
	ds_read_b128 v[134:137], v162 offset:26272
	global_load_dwordx4 v[54:57], v[158:159], off
	v_lshl_add_u64 v[158:159], v[158:159], 0, s[72:73]
	s_waitcnt lgkmcnt(5)
	v_mfma_f32_32x32x16_f16 v[2:17], v[114:117], v[50:53], v[2:17]
	s_waitcnt lgkmcnt(4)
	v_mfma_f32_32x32x16_f16 v[18:33], v[118:121], v[50:53], v[18:33]
	ds_read_b128 v[114:117], v162 offset:17600
	ds_read_b128 v[118:121], v162 offset:26304
	global_load_dwordx4 v[50:53], v[158:159], off
	v_lshl_add_u64 v[158:159], v[158:159], 0, s[72:73]
	s_waitcnt lgkmcnt(5)
	v_mfma_f32_32x32x16_f16 v[2:17], v[122:125], v[46:49], v[2:17]
	s_waitcnt lgkmcnt(4)
	v_mfma_f32_32x32x16_f16 v[18:33], v[126:129], v[46:49], v[18:33]
	ds_read_b128 v[122:125], v162 offset:17632
	ds_read_b128 v[126:129], v162 offset:26336
	global_load_dwordx4 v[46:49], v[158:159], off
	v_lshl_add_u64 v[158:159], v[158:159], 0, s[72:73]
	s_waitcnt lgkmcnt(5)
	v_mfma_f32_32x32x16_f16 v[2:17], v[130:133], v[42:45], v[2:17]
	s_waitcnt lgkmcnt(4)
	v_mfma_f32_32x32x16_f16 v[18:33], v[134:137], v[42:45], v[18:33]
	global_load_dwordx4 v[42:45], v[158:159], off
	v_lshl_add_u64 v[158:159], v[158:159], 0, s[72:73]
	s_waitcnt lgkmcnt(3)
	v_mfma_f32_32x32x16_f16 v[2:17], v[114:117], v[38:41], v[2:17]
	s_waitcnt lgkmcnt(2)
	v_mfma_f32_32x32x16_f16 v[18:33], v[118:121], v[38:41], v[18:33]
	global_load_dwordx4 v[38:41], v[158:159], off
	v_lshl_add_u64 v[158:159], v[158:159], 0, s[72:73]
	s_waitcnt lgkmcnt(1)
	v_mfma_f32_32x32x16_f16 v[2:17], v[122:125], v[34:37], v[2:17]
	s_waitcnt lgkmcnt(0)
	v_mfma_f32_32x32x16_f16 v[18:33], v[126:129], v[34:37], v[18:33]
	global_load_dwordx4 v[34:37], v[158:159], off
	v_lshl_add_u64 v[158:159], v[158:159], 0, s[72:73]
	s_waitcnt lgkmcnt(0)
	s_barrier
	ds_read_b128 v[114:117], v162 offset:34816
	ds_read_b128 v[118:121], v162 offset:43520
	ds_read_b128 v[122:125], v162 offset:34848
	ds_read_b128 v[126:129], v162 offset:43552
	ds_read_b128 v[130:133], v162 offset:34880
	ds_read_b128 v[134:137], v162 offset:43584
	s_waitcnt vmcnt(23)
	s_waitcnt lgkmcnt(5)
	v_mfma_f32_32x32x16_f16 v[2:17], v[114:117], v[94:97], v[2:17]
	s_waitcnt lgkmcnt(4)
	v_mfma_f32_32x32x16_f16 v[18:33], v[118:121], v[94:97], v[18:33]
	ds_read_b128 v[114:117], v162 offset:34912
	ds_read_b128 v[118:121], v162 offset:43616
	global_load_dwordx4 v[94:97], v[158:159], off
	v_lshl_add_u64 v[158:159], v[158:159], 0, s[72:73]
	s_waitcnt vmcnt(23)
	s_waitcnt lgkmcnt(5)
	v_mfma_f32_32x32x16_f16 v[2:17], v[122:125], v[98:101], v[2:17]
	s_waitcnt lgkmcnt(4)
	v_mfma_f32_32x32x16_f16 v[18:33], v[126:129], v[98:101], v[18:33]
	ds_read_b128 v[122:125], v162 offset:34944
	ds_read_b128 v[126:129], v162 offset:43648
	global_load_dwordx4 v[98:101], v[158:159], off
	v_lshl_add_u64 v[158:159], v[158:159], 0, s[72:73]
	s_waitcnt vmcnt(23)
	s_waitcnt lgkmcnt(5)
	v_mfma_f32_32x32x16_f16 v[2:17], v[130:133], v[102:105], v[2:17]
	s_waitcnt lgkmcnt(4)
	v_mfma_f32_32x32x16_f16 v[18:33], v[134:137], v[102:105], v[18:33]
	ds_read_b128 v[130:133], v162 offset:34976
	ds_read_b128 v[134:137], v162 offset:43680
	global_load_dwordx4 v[102:105], v[158:159], off
	v_lshl_add_u64 v[158:159], v[158:159], 0, s[72:73]
	s_waitcnt vmcnt(23)
	s_waitcnt lgkmcnt(5)
	v_mfma_f32_32x32x16_f16 v[2:17], v[114:117], v[106:109], v[2:17]
	s_waitcnt lgkmcnt(4)
	v_mfma_f32_32x32x16_f16 v[18:33], v[118:121], v[106:109], v[18:33]
	ds_read_b128 v[114:117], v162 offset:35008
	ds_read_b128 v[118:121], v162 offset:43712
	global_load_dwordx4 v[106:109], v[158:159], off
	v_lshl_add_u64 v[158:159], v[158:159], 0, s[72:73]
	s_waitcnt vmcnt(23)
	s_waitcnt lgkmcnt(5)
	v_mfma_f32_32x32x16_f16 v[2:17], v[122:125], v[142:145], v[2:17]
	s_waitcnt lgkmcnt(4)
	v_mfma_f32_32x32x16_f16 v[18:33], v[126:129], v[142:145], v[18:33]
	ds_read_b128 v[122:125], v162 offset:35040
	ds_read_b128 v[126:129], v162 offset:43744
	global_load_dwordx4 v[142:145], v[158:159], off
	v_lshl_add_u64 v[158:159], v[158:159], 0, s[72:73]
	s_waitcnt vmcnt(23)
	s_waitcnt lgkmcnt(5)
	v_mfma_f32_32x32x16_f16 v[2:17], v[130:133], v[146:149], v[2:17]
	s_waitcnt lgkmcnt(4)
	v_mfma_f32_32x32x16_f16 v[18:33], v[134:137], v[146:149], v[18:33]
	global_load_dwordx4 v[146:149], v[158:159], off
	v_lshl_add_u64 v[158:159], v[158:159], 0, s[72:73]
	s_waitcnt vmcnt(23)
	s_waitcnt lgkmcnt(3)
	v_mfma_f32_32x32x16_f16 v[2:17], v[114:117], v[150:153], v[2:17]
	s_waitcnt lgkmcnt(2)
	v_mfma_f32_32x32x16_f16 v[18:33], v[118:121], v[150:153], v[18:33]
	global_load_dwordx4 v[150:153], v[158:159], off
	v_lshl_add_u64 v[158:159], v[158:159], 0, s[72:73]
	s_waitcnt vmcnt(23)
	s_waitcnt lgkmcnt(1)
	v_mfma_f32_32x32x16_f16 v[2:17], v[122:125], v[154:157], v[2:17]
	s_waitcnt lgkmcnt(0)
	v_mfma_f32_32x32x16_f16 v[18:33], v[126:129], v[154:157], v[18:33]
	global_load_dwordx4 v[154:157], v[158:159], off
	v_lshl_add_u64 v[158:159], v[158:159], 0, s[72:73]
	s_waitcnt lgkmcnt(0)
	s_barrier
	ds_read_b128 v[114:117], v162 offset:52224
	ds_read_b128 v[118:121], v162 offset:60928
	ds_read_b128 v[122:125], v162 offset:52256
	ds_read_b128 v[126:129], v162 offset:60960
	ds_read_b128 v[130:133], v162 offset:52288
	ds_read_b128 v[134:137], v162 offset:60992
	s_waitcnt vmcnt(23)
	s_waitcnt lgkmcnt(5)
	v_mfma_f32_32x32x16_f16 v[2:17], v[114:117], v[110:113], v[2:17]
	s_waitcnt lgkmcnt(4)
	v_mfma_f32_32x32x16_f16 v[18:33], v[118:121], v[110:113], v[18:33]
	ds_read_b128 v[114:117], v162 offset:52320
	ds_read_b128 v[118:121], v162 offset:61024
	global_load_dwordx4 v[110:113], v[158:159], off
	v_lshl_add_u64 v[158:159], v[158:159], 0, s[72:73]
	s_waitcnt vmcnt(23)
	s_waitcnt lgkmcnt(5)
	v_mfma_f32_32x32x16_f16 v[2:17], v[122:125], v[90:93], v[2:17]
	s_waitcnt lgkmcnt(4)
	v_mfma_f32_32x32x16_f16 v[18:33], v[126:129], v[90:93], v[18:33]
	ds_read_b128 v[122:125], v162 offset:52352
	ds_read_b128 v[126:129], v162 offset:61056
	global_load_dwordx4 v[90:93], v[158:159], off
	v_lshl_add_u64 v[158:159], v[158:159], 0, s[72:73]
	s_waitcnt vmcnt(23)
	s_waitcnt lgkmcnt(5)
	v_mfma_f32_32x32x16_f16 v[2:17], v[130:133], v[86:89], v[2:17]
	s_waitcnt lgkmcnt(4)
	v_mfma_f32_32x32x16_f16 v[18:33], v[134:137], v[86:89], v[18:33]
	ds_read_b128 v[130:133], v162 offset:52384
	ds_read_b128 v[134:137], v162 offset:61088
	global_load_dwordx4 v[86:89], v[158:159], off
	v_lshl_add_u64 v[158:159], v[158:159], 0, s[72:73]
	s_waitcnt vmcnt(23)
	s_waitcnt lgkmcnt(5)
	v_mfma_f32_32x32x16_f16 v[2:17], v[114:117], v[82:85], v[2:17]
	s_waitcnt lgkmcnt(4)
	v_mfma_f32_32x32x16_f16 v[18:33], v[118:121], v[82:85], v[18:33]
	ds_read_b128 v[114:117], v162 offset:52416
	ds_read_b128 v[118:121], v162 offset:61120
	global_load_dwordx4 v[82:85], v[158:159], off
	v_lshl_add_u64 v[158:159], v[158:159], 0, s[72:73]
	s_waitcnt vmcnt(23)
	s_waitcnt lgkmcnt(5)
	v_mfma_f32_32x32x16_f16 v[2:17], v[122:125], v[78:81], v[2:17]
	s_waitcnt lgkmcnt(4)
	v_mfma_f32_32x32x16_f16 v[18:33], v[126:129], v[78:81], v[18:33]
	ds_read_b128 v[122:125], v162 offset:52448
	ds_read_b128 v[126:129], v162 offset:61152
	global_load_dwordx4 v[78:81], v[158:159], off
	v_lshl_add_u64 v[158:159], v[158:159], 0, s[72:73]
	s_waitcnt vmcnt(23)
	s_waitcnt lgkmcnt(5)
	v_mfma_f32_32x32x16_f16 v[2:17], v[130:133], v[74:77], v[2:17]
	s_waitcnt lgkmcnt(4)
	v_mfma_f32_32x32x16_f16 v[18:33], v[134:137], v[74:77], v[18:33]
	global_load_dwordx4 v[74:77], v[158:159], off
	v_lshl_add_u64 v[158:159], v[158:159], 0, s[72:73]
	s_waitcnt vmcnt(23)
	s_waitcnt lgkmcnt(3)
	v_mfma_f32_32x32x16_f16 v[2:17], v[114:117], v[70:73], v[2:17]
	s_waitcnt lgkmcnt(2)
	v_mfma_f32_32x32x16_f16 v[18:33], v[118:121], v[70:73], v[18:33]
	global_load_dwordx4 v[70:73], v[158:159], off
	v_lshl_add_u64 v[158:159], v[158:159], 0, s[72:73]
	s_waitcnt vmcnt(23)
	s_waitcnt lgkmcnt(1)
	v_mfma_f32_32x32x16_f16 v[2:17], v[122:125], v[66:69], v[2:17]
	s_waitcnt lgkmcnt(0)
	v_mfma_f32_32x32x16_f16 v[18:33], v[126:129], v[66:69], v[18:33]
	global_load_dwordx4 v[66:69], v[158:159], off
	v_lshl_add_u64 v[158:159], v[158:159], 0, s[72:73]
	s_waitcnt lgkmcnt(0)
	s_barrier
	ds_read_b128 v[114:117], v162 offset:0
	ds_read_b128 v[118:121], v162 offset:8704
	ds_read_b128 v[122:125], v162 offset:32
	ds_read_b128 v[126:129], v162 offset:8736
	ds_read_b128 v[130:133], v162 offset:64
	ds_read_b128 v[134:137], v162 offset:8768
	s_waitcnt vmcnt(23)
	s_waitcnt lgkmcnt(5)
	v_mfma_f32_32x32x16_f16 v[2:17], v[114:117], v[62:65], v[2:17]
	s_waitcnt lgkmcnt(4)
	v_mfma_f32_32x32x16_f16 v[18:33], v[118:121], v[62:65], v[18:33]
	ds_read_b128 v[114:117], v162 offset:96
	ds_read_b128 v[118:121], v162 offset:8800
	global_load_dwordx4 v[62:65], v[158:159], off
	v_lshl_add_u64 v[158:159], v[158:159], 0, s[72:73]
	s_waitcnt vmcnt(23)
	s_waitcnt lgkmcnt(5)
	v_mfma_f32_32x32x16_f16 v[2:17], v[122:125], v[58:61], v[2:17]
	s_waitcnt lgkmcnt(4)
	v_mfma_f32_32x32x16_f16 v[18:33], v[126:129], v[58:61], v[18:33]
	ds_read_b128 v[122:125], v162 offset:128
	ds_read_b128 v[126:129], v162 offset:8832
	global_load_dwordx4 v[58:61], v[158:159], off
	v_lshl_add_u64 v[158:159], v[158:159], 0, s[72:73]
	s_waitcnt vmcnt(23)
	s_waitcnt lgkmcnt(5)
	v_mfma_f32_32x32x16_f16 v[2:17], v[130:133], v[54:57], v[2:17]
	s_waitcnt lgkmcnt(4)
	v_mfma_f32_32x32x16_f16 v[18:33], v[134:137], v[54:57], v[18:33]
	ds_read_b128 v[130:133], v162 offset:160
	ds_read_b128 v[134:137], v162 offset:8864
	global_load_dwordx4 v[54:57], v[158:159], off
	v_lshl_add_u64 v[158:159], v[158:159], 0, s[72:73]
	s_waitcnt vmcnt(23)
	s_waitcnt lgkmcnt(5)
	v_mfma_f32_32x32x16_f16 v[2:17], v[114:117], v[50:53], v[2:17]
	s_waitcnt lgkmcnt(4)
	v_mfma_f32_32x32x16_f16 v[18:33], v[118:121], v[50:53], v[18:33]
	ds_read_b128 v[114:117], v162 offset:192
	ds_read_b128 v[118:121], v162 offset:8896
	global_load_dwordx4 v[50:53], v[158:159], off
	v_lshl_add_u64 v[158:159], v[158:159], 0, s[72:73]
	s_waitcnt vmcnt(23)
	s_waitcnt lgkmcnt(5)
	v_mfma_f32_32x32x16_f16 v[2:17], v[122:125], v[46:49], v[2:17]
	s_waitcnt lgkmcnt(4)
	v_mfma_f32_32x32x16_f16 v[18:33], v[126:129], v[46:49], v[18:33]
	ds_read_b128 v[122:125], v162 offset:224
	ds_read_b128 v[126:129], v162 offset:8928
	global_load_dwordx4 v[46:49], v[158:159], off
	v_lshl_add_u64 v[158:159], v[158:159], 0, s[72:73]
	s_waitcnt vmcnt(23)
	s_waitcnt lgkmcnt(5)
	v_mfma_f32_32x32x16_f16 v[2:17], v[130:133], v[42:45], v[2:17]
	s_waitcnt lgkmcnt(4)
	v_mfma_f32_32x32x16_f16 v[18:33], v[134:137], v[42:45], v[18:33]
	global_load_dwordx4 v[42:45], v[158:159], off
	v_lshl_add_u64 v[158:159], v[158:159], 0, s[72:73]
	s_waitcnt vmcnt(23)
	s_waitcnt lgkmcnt(3)
	v_mfma_f32_32x32x16_f16 v[2:17], v[114:117], v[38:41], v[2:17]
	s_waitcnt lgkmcnt(2)
	v_mfma_f32_32x32x16_f16 v[18:33], v[118:121], v[38:41], v[18:33]
	global_load_dwordx4 v[38:41], v[158:159], off
	v_lshl_add_u64 v[158:159], v[158:159], 0, s[72:73]
	s_waitcnt vmcnt(23)
	s_waitcnt lgkmcnt(1)
	v_mfma_f32_32x32x16_f16 v[2:17], v[122:125], v[34:37], v[2:17]
	s_waitcnt lgkmcnt(0)
	v_mfma_f32_32x32x16_f16 v[18:33], v[126:129], v[34:37], v[18:33]
	global_load_dwordx4 v[34:37], v[158:159], off
	v_lshl_add_u64 v[158:159], v[158:159], 0, s[72:73]
	s_waitcnt lgkmcnt(0)
	s_barrier
	ds_read_b128 v[114:117], v162 offset:17408
	ds_read_b128 v[118:121], v162 offset:26112
	ds_read_b128 v[122:125], v162 offset:17440
	ds_read_b128 v[126:129], v162 offset:26144
	ds_read_b128 v[130:133], v162 offset:17472
	ds_read_b128 v[134:137], v162 offset:26176
	s_waitcnt vmcnt(23)
	s_waitcnt lgkmcnt(5)
	v_mfma_f32_32x32x16_f16 v[2:17], v[114:117], v[94:97], v[2:17]
	s_waitcnt lgkmcnt(4)
	v_mfma_f32_32x32x16_f16 v[18:33], v[118:121], v[94:97], v[18:33]
	ds_read_b128 v[114:117], v162 offset:17504
	ds_read_b128 v[118:121], v162 offset:26208
	global_load_dwordx4 v[94:97], v[158:159], off
	v_lshl_add_u64 v[158:159], v[158:159], 0, s[72:73]
	s_waitcnt vmcnt(23)
	s_waitcnt lgkmcnt(5)
	v_mfma_f32_32x32x16_f16 v[2:17], v[122:125], v[98:101], v[2:17]
	s_waitcnt lgkmcnt(4)
	v_mfma_f32_32x32x16_f16 v[18:33], v[126:129], v[98:101], v[18:33]
	ds_read_b128 v[122:125], v162 offset:17536
	ds_read_b128 v[126:129], v162 offset:26240
	global_load_dwordx4 v[98:101], v[158:159], off
	v_lshl_add_u64 v[158:159], v[158:159], 0, s[72:73]
	s_waitcnt vmcnt(23)
	s_waitcnt lgkmcnt(5)
	v_mfma_f32_32x32x16_f16 v[2:17], v[130:133], v[102:105], v[2:17]
	s_waitcnt lgkmcnt(4)
	v_mfma_f32_32x32x16_f16 v[18:33], v[134:137], v[102:105], v[18:33]
	ds_read_b128 v[130:133], v162 offset:17568
	ds_read_b128 v[134:137], v162 offset:26272
	global_load_dwordx4 v[102:105], v[158:159], off
	v_lshl_add_u64 v[158:159], v[158:159], 0, s[72:73]
	s_waitcnt vmcnt(23)
	s_waitcnt lgkmcnt(5)
	v_mfma_f32_32x32x16_f16 v[2:17], v[114:117], v[106:109], v[2:17]
	s_waitcnt lgkmcnt(4)
	v_mfma_f32_32x32x16_f16 v[18:33], v[118:121], v[106:109], v[18:33]
	ds_read_b128 v[114:117], v162 offset:17600
	ds_read_b128 v[118:121], v162 offset:26304
	global_load_dwordx4 v[106:109], v[158:159], off
	v_lshl_add_u64 v[158:159], v[158:159], 0, s[72:73]
	s_waitcnt vmcnt(23)
	s_waitcnt lgkmcnt(5)
	v_mfma_f32_32x32x16_f16 v[2:17], v[122:125], v[142:145], v[2:17]
	s_waitcnt lgkmcnt(4)
	v_mfma_f32_32x32x16_f16 v[18:33], v[126:129], v[142:145], v[18:33]
	ds_read_b128 v[122:125], v162 offset:17632
	ds_read_b128 v[126:129], v162 offset:26336
	global_load_dwordx4 v[142:145], v[158:159], off
	v_lshl_add_u64 v[158:159], v[158:159], 0, s[72:73]
	s_waitcnt vmcnt(23)
	s_waitcnt lgkmcnt(5)
	v_mfma_f32_32x32x16_f16 v[2:17], v[130:133], v[146:149], v[2:17]
	s_waitcnt lgkmcnt(4)
	v_mfma_f32_32x32x16_f16 v[18:33], v[134:137], v[146:149], v[18:33]
	global_load_dwordx4 v[146:149], v[158:159], off
	v_lshl_add_u64 v[158:159], v[158:159], 0, s[72:73]
	s_waitcnt vmcnt(23)
	s_waitcnt lgkmcnt(3)
	v_mfma_f32_32x32x16_f16 v[2:17], v[114:117], v[150:153], v[2:17]
	s_waitcnt lgkmcnt(2)
	v_mfma_f32_32x32x16_f16 v[18:33], v[118:121], v[150:153], v[18:33]
	global_load_dwordx4 v[150:153], v[158:159], off
	v_lshl_add_u64 v[158:159], v[158:159], 0, s[72:73]
	s_waitcnt vmcnt(23)
	s_waitcnt lgkmcnt(1)
	v_mfma_f32_32x32x16_f16 v[2:17], v[122:125], v[154:157], v[2:17]
	s_waitcnt lgkmcnt(0)
	v_mfma_f32_32x32x16_f16 v[18:33], v[126:129], v[154:157], v[18:33]
	global_load_dwordx4 v[154:157], v[158:159], off
	v_lshl_add_u64 v[158:159], v[158:159], 0, s[72:73]
	s_waitcnt lgkmcnt(0)
	s_barrier
	ds_read_b128 v[114:117], v162 offset:34816
	ds_read_b128 v[118:121], v162 offset:43520
	ds_read_b128 v[122:125], v162 offset:34848
	ds_read_b128 v[126:129], v162 offset:43552
	ds_read_b128 v[130:133], v162 offset:34880
	ds_read_b128 v[134:137], v162 offset:43584
	s_waitcnt vmcnt(23)
	s_waitcnt lgkmcnt(5)
	v_mfma_f32_32x32x16_f16 v[2:17], v[114:117], v[110:113], v[2:17]
	s_waitcnt lgkmcnt(4)
	v_mfma_f32_32x32x16_f16 v[18:33], v[118:121], v[110:113], v[18:33]
	ds_read_b128 v[114:117], v162 offset:34912
	ds_read_b128 v[118:121], v162 offset:43616
	global_load_dwordx4 v[110:113], v[158:159], off
	v_lshl_add_u64 v[158:159], v[158:159], 0, s[72:73]
	s_waitcnt vmcnt(23)
	s_waitcnt lgkmcnt(5)
	v_mfma_f32_32x32x16_f16 v[2:17], v[122:125], v[90:93], v[2:17]
	s_waitcnt lgkmcnt(4)
	v_mfma_f32_32x32x16_f16 v[18:33], v[126:129], v[90:93], v[18:33]
	ds_read_b128 v[122:125], v162 offset:34944
	ds_read_b128 v[126:129], v162 offset:43648
	global_load_dwordx4 v[90:93], v[158:159], off
	v_lshl_add_u64 v[158:159], v[158:159], 0, s[72:73]
	s_waitcnt vmcnt(23)
	s_waitcnt lgkmcnt(5)
	v_mfma_f32_32x32x16_f16 v[2:17], v[130:133], v[86:89], v[2:17]
	s_waitcnt lgkmcnt(4)
	v_mfma_f32_32x32x16_f16 v[18:33], v[134:137], v[86:89], v[18:33]
	ds_read_b128 v[130:133], v162 offset:34976
	ds_read_b128 v[134:137], v162 offset:43680
	global_load_dwordx4 v[86:89], v[158:159], off
	v_lshl_add_u64 v[158:159], v[158:159], 0, s[72:73]
	s_waitcnt vmcnt(23)
	s_waitcnt lgkmcnt(5)
	v_mfma_f32_32x32x16_f16 v[2:17], v[114:117], v[82:85], v[2:17]
	s_waitcnt lgkmcnt(4)
	v_mfma_f32_32x32x16_f16 v[18:33], v[118:121], v[82:85], v[18:33]
	ds_read_b128 v[114:117], v162 offset:35008
	ds_read_b128 v[118:121], v162 offset:43712
	global_load_dwordx4 v[82:85], v[158:159], off
	v_lshl_add_u64 v[158:159], v[158:159], 0, s[72:73]
	s_waitcnt vmcnt(23)
	s_waitcnt lgkmcnt(5)
	v_mfma_f32_32x32x16_f16 v[2:17], v[122:125], v[78:81], v[2:17]
	s_waitcnt lgkmcnt(4)
	v_mfma_f32_32x32x16_f16 v[18:33], v[126:129], v[78:81], v[18:33]
	ds_read_b128 v[122:125], v162 offset:35040
	ds_read_b128 v[126:129], v162 offset:43744
	global_load_dwordx4 v[78:81], v[158:159], off
	v_lshl_add_u64 v[158:159], v[158:159], 0, s[72:73]
	s_waitcnt vmcnt(23)
	s_waitcnt lgkmcnt(5)
	v_mfma_f32_32x32x16_f16 v[2:17], v[130:133], v[74:77], v[2:17]
	s_waitcnt lgkmcnt(4)
	v_mfma_f32_32x32x16_f16 v[18:33], v[134:137], v[74:77], v[18:33]
	global_load_dwordx4 v[74:77], v[158:159], off
	v_lshl_add_u64 v[158:159], v[158:159], 0, s[72:73]
	s_waitcnt vmcnt(23)
	s_waitcnt lgkmcnt(3)
	v_mfma_f32_32x32x16_f16 v[2:17], v[114:117], v[70:73], v[2:17]
	s_waitcnt lgkmcnt(2)
	v_mfma_f32_32x32x16_f16 v[18:33], v[118:121], v[70:73], v[18:33]
	global_load_dwordx4 v[70:73], v[158:159], off
	v_lshl_add_u64 v[158:159], v[158:159], 0, s[72:73]
	s_waitcnt vmcnt(23)
	s_waitcnt lgkmcnt(1)
	v_mfma_f32_32x32x16_f16 v[2:17], v[122:125], v[66:69], v[2:17]
	s_waitcnt lgkmcnt(0)
	v_mfma_f32_32x32x16_f16 v[18:33], v[126:129], v[66:69], v[18:33]
	global_load_dwordx4 v[66:69], v[158:159], off
	v_lshl_add_u64 v[158:159], v[158:159], 0, s[72:73]
	s_waitcnt lgkmcnt(0)
	s_barrier
	ds_read_b128 v[114:117], v162 offset:52224
	ds_read_b128 v[118:121], v162 offset:60928
	ds_read_b128 v[122:125], v162 offset:52256
	ds_read_b128 v[126:129], v162 offset:60960
	ds_read_b128 v[130:133], v162 offset:52288
	ds_read_b128 v[134:137], v162 offset:60992
	s_waitcnt vmcnt(23)
	s_waitcnt lgkmcnt(5)
	v_mfma_f32_32x32x16_f16 v[2:17], v[114:117], v[62:65], v[2:17]
	s_waitcnt lgkmcnt(4)
	v_mfma_f32_32x32x16_f16 v[18:33], v[118:121], v[62:65], v[18:33]
	ds_read_b128 v[114:117], v162 offset:52320
	ds_read_b128 v[118:121], v162 offset:61024
	global_load_dwordx4 v[62:65], v[158:159], off
	v_lshl_add_u64 v[158:159], v[158:159], 0, s[72:73]
	s_waitcnt vmcnt(23)
	s_waitcnt lgkmcnt(5)
	v_mfma_f32_32x32x16_f16 v[2:17], v[122:125], v[58:61], v[2:17]
	s_waitcnt lgkmcnt(4)
	v_mfma_f32_32x32x16_f16 v[18:33], v[126:129], v[58:61], v[18:33]
	ds_read_b128 v[122:125], v162 offset:52352
	ds_read_b128 v[126:129], v162 offset:61056
	global_load_dwordx4 v[58:61], v[158:159], off
	v_lshl_add_u64 v[158:159], v[158:159], 0, s[72:73]
	s_waitcnt vmcnt(23)
	s_waitcnt lgkmcnt(5)
	v_mfma_f32_32x32x16_f16 v[2:17], v[130:133], v[54:57], v[2:17]
	s_waitcnt lgkmcnt(4)
	v_mfma_f32_32x32x16_f16 v[18:33], v[134:137], v[54:57], v[18:33]
	ds_read_b128 v[130:133], v162 offset:52384
	ds_read_b128 v[134:137], v162 offset:61088
	global_load_dwordx4 v[54:57], v[158:159], off
	v_lshl_add_u64 v[158:159], v[158:159], 0, s[72:73]
	s_waitcnt vmcnt(23)
	s_waitcnt lgkmcnt(5)
	v_mfma_f32_32x32x16_f16 v[2:17], v[114:117], v[50:53], v[2:17]
	s_waitcnt lgkmcnt(4)
	v_mfma_f32_32x32x16_f16 v[18:33], v[118:121], v[50:53], v[18:33]
	ds_read_b128 v[114:117], v162 offset:52416
	ds_read_b128 v[118:121], v162 offset:61120
	global_load_dwordx4 v[50:53], v[158:159], off
	v_lshl_add_u64 v[158:159], v[158:159], 0, s[72:73]
	s_waitcnt vmcnt(23)
	s_waitcnt lgkmcnt(5)
	v_mfma_f32_32x32x16_f16 v[2:17], v[122:125], v[46:49], v[2:17]
	s_waitcnt lgkmcnt(4)
	v_mfma_f32_32x32x16_f16 v[18:33], v[126:129], v[46:49], v[18:33]
	ds_read_b128 v[122:125], v162 offset:52448
	ds_read_b128 v[126:129], v162 offset:61152
	global_load_dwordx4 v[46:49], v[158:159], off
	v_lshl_add_u64 v[158:159], v[158:159], 0, s[72:73]
	s_waitcnt vmcnt(23)
	s_waitcnt lgkmcnt(5)
	v_mfma_f32_32x32x16_f16 v[2:17], v[130:133], v[42:45], v[2:17]
	s_waitcnt lgkmcnt(4)
	v_mfma_f32_32x32x16_f16 v[18:33], v[134:137], v[42:45], v[18:33]
	global_load_dwordx4 v[42:45], v[158:159], off
	v_lshl_add_u64 v[158:159], v[158:159], 0, s[72:73]
	s_waitcnt vmcnt(23)
	s_waitcnt lgkmcnt(3)
	v_mfma_f32_32x32x16_f16 v[2:17], v[114:117], v[38:41], v[2:17]
	s_waitcnt lgkmcnt(2)
	v_mfma_f32_32x32x16_f16 v[18:33], v[118:121], v[38:41], v[18:33]
	global_load_dwordx4 v[38:41], v[158:159], off
	v_lshl_add_u64 v[158:159], v[158:159], 0, s[72:73]
	s_waitcnt vmcnt(23)
	s_waitcnt lgkmcnt(1)
	v_mfma_f32_32x32x16_f16 v[2:17], v[122:125], v[34:37], v[2:17]
	s_waitcnt lgkmcnt(0)
	v_mfma_f32_32x32x16_f16 v[18:33], v[126:129], v[34:37], v[18:33]
	global_load_dwordx4 v[34:37], v[158:159], off
	v_lshl_add_u64 v[158:159], v[158:159], 0, s[72:73]
	s_waitcnt lgkmcnt(0)
	s_barrier
	ds_read_b128 v[114:117], v162 offset:0
	ds_read_b128 v[118:121], v162 offset:8704
	ds_read_b128 v[122:125], v162 offset:32
	ds_read_b128 v[126:129], v162 offset:8736
	ds_read_b128 v[130:133], v162 offset:64
	ds_read_b128 v[134:137], v162 offset:8768
	s_waitcnt vmcnt(23)
	s_waitcnt lgkmcnt(5)
	v_mfma_f32_32x32x16_f16 v[2:17], v[114:117], v[94:97], v[2:17]
	s_waitcnt lgkmcnt(4)
	v_mfma_f32_32x32x16_f16 v[18:33], v[118:121], v[94:97], v[18:33]
	ds_read_b128 v[114:117], v162 offset:96
	ds_read_b128 v[118:121], v162 offset:8800
	global_load_dwordx4 v[94:97], v[158:159], off
	v_lshl_add_u64 v[158:159], v[158:159], 0, s[72:73]
	s_waitcnt vmcnt(23)
	s_waitcnt lgkmcnt(5)
	v_mfma_f32_32x32x16_f16 v[2:17], v[122:125], v[98:101], v[2:17]
	s_waitcnt lgkmcnt(4)
	v_mfma_f32_32x32x16_f16 v[18:33], v[126:129], v[98:101], v[18:33]
	ds_read_b128 v[122:125], v162 offset:128
	ds_read_b128 v[126:129], v162 offset:8832
	global_load_dwordx4 v[98:101], v[158:159], off
	v_lshl_add_u64 v[158:159], v[158:159], 0, s[72:73]
	s_waitcnt vmcnt(23)
	s_waitcnt lgkmcnt(5)
	v_mfma_f32_32x32x16_f16 v[2:17], v[130:133], v[102:105], v[2:17]
	s_waitcnt lgkmcnt(4)
	v_mfma_f32_32x32x16_f16 v[18:33], v[134:137], v[102:105], v[18:33]
	ds_read_b128 v[130:133], v162 offset:160
	ds_read_b128 v[134:137], v162 offset:8864
	global_load_dwordx4 v[102:105], v[158:159], off
	v_lshl_add_u64 v[158:159], v[158:159], 0, s[72:73]
	s_waitcnt vmcnt(23)
	s_waitcnt lgkmcnt(5)
	v_mfma_f32_32x32x16_f16 v[2:17], v[114:117], v[106:109], v[2:17]
	s_waitcnt lgkmcnt(4)
	v_mfma_f32_32x32x16_f16 v[18:33], v[118:121], v[106:109], v[18:33]
	ds_read_b128 v[114:117], v162 offset:192
	ds_read_b128 v[118:121], v162 offset:8896
	global_load_dwordx4 v[106:109], v[158:159], off
	v_lshl_add_u64 v[158:159], v[158:159], 0, s[72:73]
	s_waitcnt vmcnt(23)
	s_waitcnt lgkmcnt(5)
	v_mfma_f32_32x32x16_f16 v[2:17], v[122:125], v[142:145], v[2:17]
	s_waitcnt lgkmcnt(4)
	v_mfma_f32_32x32x16_f16 v[18:33], v[126:129], v[142:145], v[18:33]
	ds_read_b128 v[122:125], v162 offset:224
	ds_read_b128 v[126:129], v162 offset:8928
	global_load_dwordx4 v[142:145], v[158:159], off
	v_lshl_add_u64 v[158:159], v[158:159], 0, s[72:73]
	s_waitcnt vmcnt(23)
	s_waitcnt lgkmcnt(5)
	v_mfma_f32_32x32x16_f16 v[2:17], v[130:133], v[146:149], v[2:17]
	s_waitcnt lgkmcnt(4)
	v_mfma_f32_32x32x16_f16 v[18:33], v[134:137], v[146:149], v[18:33]
	global_load_dwordx4 v[146:149], v[158:159], off
	v_lshl_add_u64 v[158:159], v[158:159], 0, s[72:73]
	s_waitcnt vmcnt(23)
	s_waitcnt lgkmcnt(3)
	v_mfma_f32_32x32x16_f16 v[2:17], v[114:117], v[150:153], v[2:17]
	s_waitcnt lgkmcnt(2)
	v_mfma_f32_32x32x16_f16 v[18:33], v[118:121], v[150:153], v[18:33]
	global_load_dwordx4 v[150:153], v[158:159], off
	v_lshl_add_u64 v[158:159], v[158:159], 0, s[72:73]
	s_waitcnt vmcnt(23)
	s_waitcnt lgkmcnt(1)
	v_mfma_f32_32x32x16_f16 v[2:17], v[122:125], v[154:157], v[2:17]
	s_waitcnt lgkmcnt(0)
	v_mfma_f32_32x32x16_f16 v[18:33], v[126:129], v[154:157], v[18:33]
	global_load_dwordx4 v[154:157], v[158:159], off
	v_lshl_add_u64 v[158:159], v[158:159], 0, s[72:73]
	s_waitcnt lgkmcnt(0)
	s_barrier
	ds_read_b128 v[114:117], v162 offset:17408
	ds_read_b128 v[118:121], v162 offset:26112
	ds_read_b128 v[122:125], v162 offset:17440
	ds_read_b128 v[126:129], v162 offset:26144
	ds_read_b128 v[130:133], v162 offset:17472
	ds_read_b128 v[134:137], v162 offset:26176
	s_waitcnt vmcnt(23)
	s_waitcnt lgkmcnt(5)
	v_mfma_f32_32x32x16_f16 v[2:17], v[114:117], v[110:113], v[2:17]
	s_waitcnt lgkmcnt(4)
	v_mfma_f32_32x32x16_f16 v[18:33], v[118:121], v[110:113], v[18:33]
	ds_read_b128 v[114:117], v162 offset:17504
	ds_read_b128 v[118:121], v162 offset:26208
	global_load_dwordx4 v[110:113], v[158:159], off
	v_lshl_add_u64 v[158:159], v[158:159], 0, s[72:73]
	s_waitcnt vmcnt(23)
	s_waitcnt lgkmcnt(5)
	v_mfma_f32_32x32x16_f16 v[2:17], v[122:125], v[90:93], v[2:17]
	s_waitcnt lgkmcnt(4)
	v_mfma_f32_32x32x16_f16 v[18:33], v[126:129], v[90:93], v[18:33]
	ds_read_b128 v[122:125], v162 offset:17536
	ds_read_b128 v[126:129], v162 offset:26240
	global_load_dwordx4 v[90:93], v[158:159], off
	v_lshl_add_u64 v[158:159], v[158:159], 0, s[72:73]
	s_waitcnt vmcnt(23)
	s_waitcnt lgkmcnt(5)
	v_mfma_f32_32x32x16_f16 v[2:17], v[130:133], v[86:89], v[2:17]
	s_waitcnt lgkmcnt(4)
	v_mfma_f32_32x32x16_f16 v[18:33], v[134:137], v[86:89], v[18:33]
	ds_read_b128 v[130:133], v162 offset:17568
	ds_read_b128 v[134:137], v162 offset:26272
	global_load_dwordx4 v[86:89], v[158:159], off
	v_lshl_add_u64 v[158:159], v[158:159], 0, s[72:73]
	s_waitcnt vmcnt(23)
	s_waitcnt lgkmcnt(5)
	v_mfma_f32_32x32x16_f16 v[2:17], v[114:117], v[82:85], v[2:17]
	s_waitcnt lgkmcnt(4)
	v_mfma_f32_32x32x16_f16 v[18:33], v[118:121], v[82:85], v[18:33]
	ds_read_b128 v[114:117], v162 offset:17600
	ds_read_b128 v[118:121], v162 offset:26304
	global_load_dwordx4 v[82:85], v[158:159], off
	v_lshl_add_u64 v[158:159], v[158:159], 0, s[72:73]
	s_waitcnt vmcnt(23)
	s_waitcnt lgkmcnt(5)
	v_mfma_f32_32x32x16_f16 v[2:17], v[122:125], v[78:81], v[2:17]
	s_waitcnt lgkmcnt(4)
	v_mfma_f32_32x32x16_f16 v[18:33], v[126:129], v[78:81], v[18:33]
	ds_read_b128 v[122:125], v162 offset:17632
	ds_read_b128 v[126:129], v162 offset:26336
	global_load_dwordx4 v[78:81], v[158:159], off
	v_lshl_add_u64 v[158:159], v[158:159], 0, s[72:73]
	s_waitcnt vmcnt(23)
	s_waitcnt lgkmcnt(5)
	v_mfma_f32_32x32x16_f16 v[2:17], v[130:133], v[74:77], v[2:17]
	s_waitcnt lgkmcnt(4)
	v_mfma_f32_32x32x16_f16 v[18:33], v[134:137], v[74:77], v[18:33]
	global_load_dwordx4 v[74:77], v[158:159], off
	v_lshl_add_u64 v[158:159], v[158:159], 0, s[72:73]
	s_waitcnt vmcnt(23)
	s_waitcnt lgkmcnt(3)
	v_mfma_f32_32x32x16_f16 v[2:17], v[114:117], v[70:73], v[2:17]
	s_waitcnt lgkmcnt(2)
	v_mfma_f32_32x32x16_f16 v[18:33], v[118:121], v[70:73], v[18:33]
	global_load_dwordx4 v[70:73], v[158:159], off
	v_lshl_add_u64 v[158:159], v[158:159], 0, s[72:73]
	s_waitcnt vmcnt(23)
	s_waitcnt lgkmcnt(1)
	v_mfma_f32_32x32x16_f16 v[2:17], v[122:125], v[66:69], v[2:17]
	s_waitcnt lgkmcnt(0)
	v_mfma_f32_32x32x16_f16 v[18:33], v[126:129], v[66:69], v[18:33]
	global_load_dwordx4 v[66:69], v[158:159], off
	v_lshl_add_u64 v[158:159], v[158:159], 0, s[72:73]
	s_waitcnt lgkmcnt(0)
	s_barrier
	ds_read_b128 v[114:117], v162 offset:34816
	ds_read_b128 v[118:121], v162 offset:43520
	ds_read_b128 v[122:125], v162 offset:34848
	ds_read_b128 v[126:129], v162 offset:43552
	ds_read_b128 v[130:133], v162 offset:34880
	ds_read_b128 v[134:137], v162 offset:43584
	s_waitcnt vmcnt(23)
	s_waitcnt lgkmcnt(5)
	v_mfma_f32_32x32x16_f16 v[2:17], v[114:117], v[62:65], v[2:17]
	s_waitcnt lgkmcnt(4)
	v_mfma_f32_32x32x16_f16 v[18:33], v[118:121], v[62:65], v[18:33]
	ds_read_b128 v[114:117], v162 offset:34912
	ds_read_b128 v[118:121], v162 offset:43616
	global_load_dwordx4 v[62:65], v[158:159], off
	v_lshl_add_u64 v[158:159], v[158:159], 0, s[72:73]
	s_waitcnt vmcnt(23)
	s_waitcnt lgkmcnt(5)
	v_mfma_f32_32x32x16_f16 v[2:17], v[122:125], v[58:61], v[2:17]
	s_waitcnt lgkmcnt(4)
	v_mfma_f32_32x32x16_f16 v[18:33], v[126:129], v[58:61], v[18:33]
	ds_read_b128 v[122:125], v162 offset:34944
	ds_read_b128 v[126:129], v162 offset:43648
	global_load_dwordx4 v[58:61], v[158:159], off
	v_lshl_add_u64 v[158:159], v[158:159], 0, s[72:73]
	s_waitcnt vmcnt(23)
	s_waitcnt lgkmcnt(5)
	v_mfma_f32_32x32x16_f16 v[2:17], v[130:133], v[54:57], v[2:17]
	s_waitcnt lgkmcnt(4)
	v_mfma_f32_32x32x16_f16 v[18:33], v[134:137], v[54:57], v[18:33]
	ds_read_b128 v[130:133], v162 offset:34976
	ds_read_b128 v[134:137], v162 offset:43680
	global_load_dwordx4 v[54:57], v[158:159], off
	v_lshl_add_u64 v[158:159], v[158:159], 0, s[72:73]
	s_waitcnt vmcnt(23)
	s_waitcnt lgkmcnt(5)
	v_mfma_f32_32x32x16_f16 v[2:17], v[114:117], v[50:53], v[2:17]
	s_waitcnt lgkmcnt(4)
	v_mfma_f32_32x32x16_f16 v[18:33], v[118:121], v[50:53], v[18:33]
	ds_read_b128 v[114:117], v162 offset:35008
	ds_read_b128 v[118:121], v162 offset:43712
	global_load_dwordx4 v[50:53], v[158:159], off
	v_lshl_add_u64 v[158:159], v[158:159], 0, s[72:73]
	s_waitcnt vmcnt(23)
	s_waitcnt lgkmcnt(5)
	v_mfma_f32_32x32x16_f16 v[2:17], v[122:125], v[46:49], v[2:17]
	s_waitcnt lgkmcnt(4)
	v_mfma_f32_32x32x16_f16 v[18:33], v[126:129], v[46:49], v[18:33]
	ds_read_b128 v[122:125], v162 offset:35040
	ds_read_b128 v[126:129], v162 offset:43744
	global_load_dwordx4 v[46:49], v[158:159], off
	v_lshl_add_u64 v[158:159], v[158:159], 0, s[72:73]
	s_waitcnt vmcnt(23)
	s_waitcnt lgkmcnt(5)
	v_mfma_f32_32x32x16_f16 v[2:17], v[130:133], v[42:45], v[2:17]
	s_waitcnt lgkmcnt(4)
	v_mfma_f32_32x32x16_f16 v[18:33], v[134:137], v[42:45], v[18:33]
	global_load_dwordx4 v[42:45], v[158:159], off
	v_lshl_add_u64 v[158:159], v[158:159], 0, s[72:73]
	s_waitcnt vmcnt(23)
	s_waitcnt lgkmcnt(3)
	v_mfma_f32_32x32x16_f16 v[2:17], v[114:117], v[38:41], v[2:17]
	s_waitcnt lgkmcnt(2)
	v_mfma_f32_32x32x16_f16 v[18:33], v[118:121], v[38:41], v[18:33]
	global_load_dwordx4 v[38:41], v[158:159], off
	v_lshl_add_u64 v[158:159], v[158:159], 0, s[72:73]
	s_waitcnt vmcnt(23)
	s_waitcnt lgkmcnt(1)
	v_mfma_f32_32x32x16_f16 v[2:17], v[122:125], v[34:37], v[2:17]
	s_waitcnt lgkmcnt(0)
	v_mfma_f32_32x32x16_f16 v[18:33], v[126:129], v[34:37], v[18:33]
	global_load_dwordx4 v[34:37], v[158:159], off
	v_lshl_add_u64 v[158:159], v[158:159], 0, s[72:73]
	s_waitcnt lgkmcnt(0)
	s_barrier
	ds_read_b128 v[114:117], v162 offset:52224
	ds_read_b128 v[118:121], v162 offset:60928
	ds_read_b128 v[122:125], v162 offset:52256
	ds_read_b128 v[126:129], v162 offset:60960
	ds_read_b128 v[130:133], v162 offset:52288
	ds_read_b128 v[134:137], v162 offset:60992
	s_waitcnt vmcnt(23)
	s_waitcnt lgkmcnt(5)
	v_mfma_f32_32x32x16_f16 v[2:17], v[114:117], v[94:97], v[2:17]
	s_waitcnt lgkmcnt(4)
	v_mfma_f32_32x32x16_f16 v[18:33], v[118:121], v[94:97], v[18:33]
	ds_read_b128 v[114:117], v162 offset:52320
	ds_read_b128 v[118:121], v162 offset:61024
	global_load_dwordx4 v[94:97], v[158:159], off
	v_lshl_add_u64 v[158:159], v[158:159], 0, s[72:73]
	s_waitcnt vmcnt(23)
	s_waitcnt lgkmcnt(5)
	v_mfma_f32_32x32x16_f16 v[2:17], v[122:125], v[98:101], v[2:17]
	s_waitcnt lgkmcnt(4)
	v_mfma_f32_32x32x16_f16 v[18:33], v[126:129], v[98:101], v[18:33]
	ds_read_b128 v[122:125], v162 offset:52352
	ds_read_b128 v[126:129], v162 offset:61056
	global_load_dwordx4 v[98:101], v[158:159], off
	v_lshl_add_u64 v[158:159], v[158:159], 0, s[72:73]
	s_waitcnt vmcnt(23)
	s_waitcnt lgkmcnt(5)
	v_mfma_f32_32x32x16_f16 v[2:17], v[130:133], v[102:105], v[2:17]
	s_waitcnt lgkmcnt(4)
	v_mfma_f32_32x32x16_f16 v[18:33], v[134:137], v[102:105], v[18:33]
	ds_read_b128 v[130:133], v162 offset:52384
	ds_read_b128 v[134:137], v162 offset:61088
	global_load_dwordx4 v[102:105], v[158:159], off
	v_lshl_add_u64 v[158:159], v[158:159], 0, s[72:73]
	s_waitcnt vmcnt(23)
	s_waitcnt lgkmcnt(5)
	v_mfma_f32_32x32x16_f16 v[2:17], v[114:117], v[106:109], v[2:17]
	s_waitcnt lgkmcnt(4)
	v_mfma_f32_32x32x16_f16 v[18:33], v[118:121], v[106:109], v[18:33]
	ds_read_b128 v[114:117], v162 offset:52416
	ds_read_b128 v[118:121], v162 offset:61120
	global_load_dwordx4 v[106:109], v[158:159], off
	v_lshl_add_u64 v[158:159], v[158:159], 0, s[72:73]
	s_waitcnt vmcnt(23)
	s_waitcnt lgkmcnt(5)
	v_mfma_f32_32x32x16_f16 v[2:17], v[122:125], v[142:145], v[2:17]
	s_waitcnt lgkmcnt(4)
	v_mfma_f32_32x32x16_f16 v[18:33], v[126:129], v[142:145], v[18:33]
	ds_read_b128 v[122:125], v162 offset:52448
	ds_read_b128 v[126:129], v162 offset:61152
	global_load_dwordx4 v[142:145], v[158:159], off
	v_lshl_add_u64 v[158:159], v[158:159], 0, s[72:73]
	s_waitcnt vmcnt(23)
	s_waitcnt lgkmcnt(5)
	v_mfma_f32_32x32x16_f16 v[2:17], v[130:133], v[146:149], v[2:17]
	s_waitcnt lgkmcnt(4)
	v_mfma_f32_32x32x16_f16 v[18:33], v[134:137], v[146:149], v[18:33]
	global_load_dwordx4 v[146:149], v[158:159], off
	v_lshl_add_u64 v[158:159], v[158:159], 0, s[72:73]
	s_waitcnt vmcnt(23)
	s_waitcnt lgkmcnt(3)
	v_mfma_f32_32x32x16_f16 v[2:17], v[114:117], v[150:153], v[2:17]
	s_waitcnt lgkmcnt(2)
	v_mfma_f32_32x32x16_f16 v[18:33], v[118:121], v[150:153], v[18:33]
	global_load_dwordx4 v[150:153], v[158:159], off
	v_lshl_add_u64 v[158:159], v[158:159], 0, s[72:73]
	s_waitcnt vmcnt(23)
	s_waitcnt lgkmcnt(1)
	v_mfma_f32_32x32x16_f16 v[2:17], v[122:125], v[154:157], v[2:17]
	s_waitcnt lgkmcnt(0)
	v_mfma_f32_32x32x16_f16 v[18:33], v[126:129], v[154:157], v[18:33]
	global_load_dwordx4 v[154:157], v[158:159], off
	v_lshl_add_u64 v[158:159], v[158:159], 0, s[72:73]
	s_waitcnt lgkmcnt(0)
	s_barrier
	ds_read_b128 v[114:117], v162 offset:0
	ds_read_b128 v[118:121], v162 offset:8704
	ds_read_b128 v[122:125], v162 offset:32
	ds_read_b128 v[126:129], v162 offset:8736
	ds_read_b128 v[130:133], v162 offset:64
	ds_read_b128 v[134:137], v162 offset:8768
	s_waitcnt vmcnt(23)
	s_waitcnt lgkmcnt(5)
	v_mfma_f32_32x32x16_f16 v[2:17], v[114:117], v[110:113], v[2:17]
	s_waitcnt lgkmcnt(4)
	v_mfma_f32_32x32x16_f16 v[18:33], v[118:121], v[110:113], v[18:33]
	ds_read_b128 v[114:117], v162 offset:96
	ds_read_b128 v[118:121], v162 offset:8800
	global_load_dwordx4 v[110:113], v[158:159], off
	v_lshl_add_u64 v[158:159], v[158:159], 0, s[72:73]
	s_waitcnt vmcnt(23)
	s_waitcnt lgkmcnt(5)
	v_mfma_f32_32x32x16_f16 v[2:17], v[122:125], v[90:93], v[2:17]
	s_waitcnt lgkmcnt(4)
	v_mfma_f32_32x32x16_f16 v[18:33], v[126:129], v[90:93], v[18:33]
	ds_read_b128 v[122:125], v162 offset:128
	ds_read_b128 v[126:129], v162 offset:8832
	global_load_dwordx4 v[90:93], v[158:159], off
	v_lshl_add_u64 v[158:159], v[158:159], 0, s[72:73]
	s_waitcnt vmcnt(23)
	s_waitcnt lgkmcnt(5)
	v_mfma_f32_32x32x16_f16 v[2:17], v[130:133], v[86:89], v[2:17]
	s_waitcnt lgkmcnt(4)
	v_mfma_f32_32x32x16_f16 v[18:33], v[134:137], v[86:89], v[18:33]
	ds_read_b128 v[130:133], v162 offset:160
	ds_read_b128 v[134:137], v162 offset:8864
	global_load_dwordx4 v[86:89], v[158:159], off
	v_lshl_add_u64 v[158:159], v[158:159], 0, s[72:73]
	s_waitcnt vmcnt(23)
	s_waitcnt lgkmcnt(5)
	v_mfma_f32_32x32x16_f16 v[2:17], v[114:117], v[82:85], v[2:17]
	s_waitcnt lgkmcnt(4)
	v_mfma_f32_32x32x16_f16 v[18:33], v[118:121], v[82:85], v[18:33]
	ds_read_b128 v[114:117], v162 offset:192
	ds_read_b128 v[118:121], v162 offset:8896
	global_load_dwordx4 v[82:85], v[158:159], off
	v_lshl_add_u64 v[158:159], v[158:159], 0, s[72:73]
	s_waitcnt vmcnt(23)
	s_waitcnt lgkmcnt(5)
	v_mfma_f32_32x32x16_f16 v[2:17], v[122:125], v[78:81], v[2:17]
	s_waitcnt lgkmcnt(4)
	v_mfma_f32_32x32x16_f16 v[18:33], v[126:129], v[78:81], v[18:33]
	ds_read_b128 v[122:125], v162 offset:224
	ds_read_b128 v[126:129], v162 offset:8928
	global_load_dwordx4 v[78:81], v[158:159], off
	v_lshl_add_u64 v[158:159], v[158:159], 0, s[72:73]
	s_waitcnt vmcnt(23)
	s_waitcnt lgkmcnt(5)
	v_mfma_f32_32x32x16_f16 v[2:17], v[130:133], v[74:77], v[2:17]
	s_waitcnt lgkmcnt(4)
	v_mfma_f32_32x32x16_f16 v[18:33], v[134:137], v[74:77], v[18:33]
	global_load_dwordx4 v[74:77], v[158:159], off
	v_lshl_add_u64 v[158:159], v[158:159], 0, s[72:73]
	s_waitcnt vmcnt(23)
	s_waitcnt lgkmcnt(3)
	v_mfma_f32_32x32x16_f16 v[2:17], v[114:117], v[70:73], v[2:17]
	s_waitcnt lgkmcnt(2)
	v_mfma_f32_32x32x16_f16 v[18:33], v[118:121], v[70:73], v[18:33]
	global_load_dwordx4 v[70:73], v[158:159], off
	v_lshl_add_u64 v[158:159], v[158:159], 0, s[72:73]
	s_waitcnt vmcnt(23)
	s_waitcnt lgkmcnt(1)
	v_mfma_f32_32x32x16_f16 v[2:17], v[122:125], v[66:69], v[2:17]
	s_waitcnt lgkmcnt(0)
	v_mfma_f32_32x32x16_f16 v[18:33], v[126:129], v[66:69], v[18:33]
	global_load_dwordx4 v[66:69], v[158:159], off
	v_lshl_add_u64 v[158:159], v[158:159], 0, s[72:73]
	s_waitcnt lgkmcnt(0)
	s_barrier
	ds_read_b128 v[114:117], v162 offset:17408
	ds_read_b128 v[118:121], v162 offset:26112
	ds_read_b128 v[122:125], v162 offset:17440
	ds_read_b128 v[126:129], v162 offset:26144
	ds_read_b128 v[130:133], v162 offset:17472
	ds_read_b128 v[134:137], v162 offset:26176
	s_waitcnt vmcnt(23)
	s_waitcnt lgkmcnt(5)
	v_mfma_f32_32x32x16_f16 v[2:17], v[114:117], v[62:65], v[2:17]
	s_waitcnt lgkmcnt(4)
	v_mfma_f32_32x32x16_f16 v[18:33], v[118:121], v[62:65], v[18:33]
	ds_read_b128 v[114:117], v162 offset:17504
	ds_read_b128 v[118:121], v162 offset:26208
	global_load_dwordx4 v[62:65], v[158:159], off
	v_lshl_add_u64 v[158:159], v[158:159], 0, s[72:73]
	s_waitcnt vmcnt(23)
	s_waitcnt lgkmcnt(5)
	v_mfma_f32_32x32x16_f16 v[2:17], v[122:125], v[58:61], v[2:17]
	s_waitcnt lgkmcnt(4)
	v_mfma_f32_32x32x16_f16 v[18:33], v[126:129], v[58:61], v[18:33]
	ds_read_b128 v[122:125], v162 offset:17536
	ds_read_b128 v[126:129], v162 offset:26240
	global_load_dwordx4 v[58:61], v[158:159], off
	v_lshl_add_u64 v[158:159], v[158:159], 0, s[72:73]
	s_waitcnt vmcnt(23)
	s_waitcnt lgkmcnt(5)
	v_mfma_f32_32x32x16_f16 v[2:17], v[130:133], v[54:57], v[2:17]
	s_waitcnt lgkmcnt(4)
	v_mfma_f32_32x32x16_f16 v[18:33], v[134:137], v[54:57], v[18:33]
	ds_read_b128 v[130:133], v162 offset:17568
	ds_read_b128 v[134:137], v162 offset:26272
	global_load_dwordx4 v[54:57], v[158:159], off
	v_lshl_add_u64 v[158:159], v[158:159], 0, s[72:73]
	s_waitcnt vmcnt(23)
	s_waitcnt lgkmcnt(5)
	v_mfma_f32_32x32x16_f16 v[2:17], v[114:117], v[50:53], v[2:17]
	s_waitcnt lgkmcnt(4)
	v_mfma_f32_32x32x16_f16 v[18:33], v[118:121], v[50:53], v[18:33]
	ds_read_b128 v[114:117], v162 offset:17600
	ds_read_b128 v[118:121], v162 offset:26304
	global_load_dwordx4 v[50:53], v[158:159], off
	v_lshl_add_u64 v[158:159], v[158:159], 0, s[72:73]
	s_waitcnt vmcnt(23)
	s_waitcnt lgkmcnt(5)
	v_mfma_f32_32x32x16_f16 v[2:17], v[122:125], v[46:49], v[2:17]
	s_waitcnt lgkmcnt(4)
	v_mfma_f32_32x32x16_f16 v[18:33], v[126:129], v[46:49], v[18:33]
	ds_read_b128 v[122:125], v162 offset:17632
	ds_read_b128 v[126:129], v162 offset:26336
	global_load_dwordx4 v[46:49], v[158:159], off
	v_lshl_add_u64 v[158:159], v[158:159], 0, s[72:73]
	s_waitcnt vmcnt(23)
	s_waitcnt lgkmcnt(5)
	v_mfma_f32_32x32x16_f16 v[2:17], v[130:133], v[42:45], v[2:17]
	s_waitcnt lgkmcnt(4)
	v_mfma_f32_32x32x16_f16 v[18:33], v[134:137], v[42:45], v[18:33]
	global_load_dwordx4 v[42:45], v[158:159], off
	v_lshl_add_u64 v[158:159], v[158:159], 0, s[72:73]
	s_waitcnt vmcnt(23)
	s_waitcnt lgkmcnt(3)
	v_mfma_f32_32x32x16_f16 v[2:17], v[114:117], v[38:41], v[2:17]
	s_waitcnt lgkmcnt(2)
	v_mfma_f32_32x32x16_f16 v[18:33], v[118:121], v[38:41], v[18:33]
	global_load_dwordx4 v[38:41], v[158:159], off
	v_lshl_add_u64 v[158:159], v[158:159], 0, s[72:73]
	s_waitcnt vmcnt(23)
	s_waitcnt lgkmcnt(1)
	v_mfma_f32_32x32x16_f16 v[2:17], v[122:125], v[34:37], v[2:17]
	s_waitcnt lgkmcnt(0)
	v_mfma_f32_32x32x16_f16 v[18:33], v[126:129], v[34:37], v[18:33]
	global_load_dwordx4 v[34:37], v[158:159], off
	v_lshl_add_u64 v[158:159], v[158:159], 0, s[72:73]
	s_waitcnt lgkmcnt(0)
	s_barrier
	ds_read_b128 v[114:117], v162 offset:34816
	ds_read_b128 v[118:121], v162 offset:43520
	ds_read_b128 v[122:125], v162 offset:34848
	ds_read_b128 v[126:129], v162 offset:43552
	ds_read_b128 v[130:133], v162 offset:34880
	ds_read_b128 v[134:137], v162 offset:43584
	s_waitcnt vmcnt(23)
	s_waitcnt lgkmcnt(5)
	v_mfma_f32_32x32x16_f16 v[2:17], v[114:117], v[94:97], v[2:17]
	s_waitcnt lgkmcnt(4)
	v_mfma_f32_32x32x16_f16 v[18:33], v[118:121], v[94:97], v[18:33]
	ds_read_b128 v[114:117], v162 offset:34912
	ds_read_b128 v[118:121], v162 offset:43616
	global_load_dwordx4 v[94:97], v[158:159], off
	v_lshl_add_u64 v[158:159], v[158:159], 0, s[72:73]
	s_waitcnt vmcnt(23)
	s_waitcnt lgkmcnt(5)
	v_mfma_f32_32x32x16_f16 v[2:17], v[122:125], v[98:101], v[2:17]
	s_waitcnt lgkmcnt(4)
	v_mfma_f32_32x32x16_f16 v[18:33], v[126:129], v[98:101], v[18:33]
	ds_read_b128 v[122:125], v162 offset:34944
	ds_read_b128 v[126:129], v162 offset:43648
	global_load_dwordx4 v[98:101], v[158:159], off
	v_lshl_add_u64 v[158:159], v[158:159], 0, s[72:73]
	s_waitcnt vmcnt(23)
	s_waitcnt lgkmcnt(5)
	v_mfma_f32_32x32x16_f16 v[2:17], v[130:133], v[102:105], v[2:17]
	s_waitcnt lgkmcnt(4)
	v_mfma_f32_32x32x16_f16 v[18:33], v[134:137], v[102:105], v[18:33]
	ds_read_b128 v[130:133], v162 offset:34976
	ds_read_b128 v[134:137], v162 offset:43680
	global_load_dwordx4 v[102:105], v[158:159], off
	v_lshl_add_u64 v[158:159], v[158:159], 0, s[72:73]
	s_waitcnt vmcnt(23)
	s_waitcnt lgkmcnt(5)
	v_mfma_f32_32x32x16_f16 v[2:17], v[114:117], v[106:109], v[2:17]
	s_waitcnt lgkmcnt(4)
	v_mfma_f32_32x32x16_f16 v[18:33], v[118:121], v[106:109], v[18:33]
	ds_read_b128 v[114:117], v162 offset:35008
	ds_read_b128 v[118:121], v162 offset:43712
	global_load_dwordx4 v[106:109], v[158:159], off
	v_lshl_add_u64 v[158:159], v[158:159], 0, s[72:73]
	s_waitcnt vmcnt(23)
	s_waitcnt lgkmcnt(5)
	v_mfma_f32_32x32x16_f16 v[2:17], v[122:125], v[142:145], v[2:17]
	s_waitcnt lgkmcnt(4)
	v_mfma_f32_32x32x16_f16 v[18:33], v[126:129], v[142:145], v[18:33]
	ds_read_b128 v[122:125], v162 offset:35040
	ds_read_b128 v[126:129], v162 offset:43744
	global_load_dwordx4 v[142:145], v[158:159], off
	v_lshl_add_u64 v[158:159], v[158:159], 0, s[72:73]
	s_waitcnt vmcnt(23)
	s_waitcnt lgkmcnt(5)
	v_mfma_f32_32x32x16_f16 v[2:17], v[130:133], v[146:149], v[2:17]
	s_waitcnt lgkmcnt(4)
	v_mfma_f32_32x32x16_f16 v[18:33], v[134:137], v[146:149], v[18:33]
	global_load_dwordx4 v[146:149], v[158:159], off
	v_lshl_add_u64 v[158:159], v[158:159], 0, s[72:73]
	s_waitcnt vmcnt(23)
	s_waitcnt lgkmcnt(3)
	v_mfma_f32_32x32x16_f16 v[2:17], v[114:117], v[150:153], v[2:17]
	s_waitcnt lgkmcnt(2)
	v_mfma_f32_32x32x16_f16 v[18:33], v[118:121], v[150:153], v[18:33]
	global_load_dwordx4 v[150:153], v[158:159], off
	v_lshl_add_u64 v[158:159], v[158:159], 0, s[72:73]
	s_waitcnt vmcnt(23)
	s_waitcnt lgkmcnt(1)
	v_mfma_f32_32x32x16_f16 v[2:17], v[122:125], v[154:157], v[2:17]
	s_waitcnt lgkmcnt(0)
	v_mfma_f32_32x32x16_f16 v[18:33], v[126:129], v[154:157], v[18:33]
	global_load_dwordx4 v[154:157], v[158:159], off
	v_lshl_add_u64 v[158:159], v[158:159], 0, s[72:73]
	s_waitcnt lgkmcnt(0)
	s_barrier
	ds_read_b128 v[114:117], v162 offset:52224
	ds_read_b128 v[118:121], v162 offset:60928
	ds_read_b128 v[122:125], v162 offset:52256
	ds_read_b128 v[126:129], v162 offset:60960
	ds_read_b128 v[130:133], v162 offset:52288
	ds_read_b128 v[134:137], v162 offset:60992
	s_waitcnt vmcnt(23)
	s_waitcnt lgkmcnt(5)
	v_mfma_f32_32x32x16_f16 v[2:17], v[114:117], v[110:113], v[2:17]
	s_waitcnt lgkmcnt(4)
	v_mfma_f32_32x32x16_f16 v[18:33], v[118:121], v[110:113], v[18:33]
	ds_read_b128 v[114:117], v162 offset:52320
	ds_read_b128 v[118:121], v162 offset:61024
	global_load_dwordx4 v[110:113], v[158:159], off
	v_lshl_add_u64 v[158:159], v[158:159], 0, s[72:73]
	s_waitcnt vmcnt(23)
	s_waitcnt lgkmcnt(5)
	v_mfma_f32_32x32x16_f16 v[2:17], v[122:125], v[90:93], v[2:17]
	s_waitcnt lgkmcnt(4)
	v_mfma_f32_32x32x16_f16 v[18:33], v[126:129], v[90:93], v[18:33]
	ds_read_b128 v[122:125], v162 offset:52352
	ds_read_b128 v[126:129], v162 offset:61056
	global_load_dwordx4 v[90:93], v[158:159], off
	v_lshl_add_u64 v[158:159], v[158:159], 0, s[72:73]
	s_waitcnt vmcnt(23)
	s_waitcnt lgkmcnt(5)
	v_mfma_f32_32x32x16_f16 v[2:17], v[130:133], v[86:89], v[2:17]
	s_waitcnt lgkmcnt(4)
	v_mfma_f32_32x32x16_f16 v[18:33], v[134:137], v[86:89], v[18:33]
	ds_read_b128 v[130:133], v162 offset:52384
	ds_read_b128 v[134:137], v162 offset:61088
	global_load_dwordx4 v[86:89], v[158:159], off
	v_lshl_add_u64 v[158:159], v[158:159], 0, s[72:73]
	s_waitcnt vmcnt(23)
	s_waitcnt lgkmcnt(5)
	v_mfma_f32_32x32x16_f16 v[2:17], v[114:117], v[82:85], v[2:17]
	s_waitcnt lgkmcnt(4)
	v_mfma_f32_32x32x16_f16 v[18:33], v[118:121], v[82:85], v[18:33]
	ds_read_b128 v[114:117], v162 offset:52416
	ds_read_b128 v[118:121], v162 offset:61120
	global_load_dwordx4 v[82:85], v[158:159], off
	v_lshl_add_u64 v[158:159], v[158:159], 0, s[72:73]
	s_waitcnt vmcnt(23)
	s_waitcnt lgkmcnt(5)
	v_mfma_f32_32x32x16_f16 v[2:17], v[122:125], v[78:81], v[2:17]
	s_waitcnt lgkmcnt(4)
	v_mfma_f32_32x32x16_f16 v[18:33], v[126:129], v[78:81], v[18:33]
	ds_read_b128 v[122:125], v162 offset:52448
	ds_read_b128 v[126:129], v162 offset:61152
	global_load_dwordx4 v[78:81], v[158:159], off
	v_lshl_add_u64 v[158:159], v[158:159], 0, s[72:73]
	s_waitcnt vmcnt(23)
	s_waitcnt lgkmcnt(5)
	v_mfma_f32_32x32x16_f16 v[2:17], v[130:133], v[74:77], v[2:17]
	s_waitcnt lgkmcnt(4)
	v_mfma_f32_32x32x16_f16 v[18:33], v[134:137], v[74:77], v[18:33]
	global_load_dwordx4 v[74:77], v[158:159], off
	v_lshl_add_u64 v[158:159], v[158:159], 0, s[72:73]
	s_waitcnt vmcnt(23)
	s_waitcnt lgkmcnt(3)
	v_mfma_f32_32x32x16_f16 v[2:17], v[114:117], v[70:73], v[2:17]
	s_waitcnt lgkmcnt(2)
	v_mfma_f32_32x32x16_f16 v[18:33], v[118:121], v[70:73], v[18:33]
	global_load_dwordx4 v[70:73], v[158:159], off
	v_lshl_add_u64 v[158:159], v[158:159], 0, s[72:73]
	s_waitcnt vmcnt(23)
	s_waitcnt lgkmcnt(1)
	v_mfma_f32_32x32x16_f16 v[2:17], v[122:125], v[66:69], v[2:17]
	s_waitcnt lgkmcnt(0)
	v_mfma_f32_32x32x16_f16 v[18:33], v[126:129], v[66:69], v[18:33]
	global_load_dwordx4 v[66:69], v[158:159], off
	v_lshl_add_u64 v[158:159], v[158:159], 0, s[72:73]
	s_waitcnt lgkmcnt(0)
	s_barrier
	ds_read_b128 v[114:117], v162 offset:0
	ds_read_b128 v[118:121], v162 offset:8704
	ds_read_b128 v[122:125], v162 offset:32
	ds_read_b128 v[126:129], v162 offset:8736
	ds_read_b128 v[130:133], v162 offset:64
	ds_read_b128 v[134:137], v162 offset:8768
	s_waitcnt vmcnt(23)
	s_waitcnt lgkmcnt(5)
	v_mfma_f32_32x32x16_f16 v[2:17], v[114:117], v[62:65], v[2:17]
	s_waitcnt lgkmcnt(4)
	v_mfma_f32_32x32x16_f16 v[18:33], v[118:121], v[62:65], v[18:33]
	ds_read_b128 v[114:117], v162 offset:96
	ds_read_b128 v[118:121], v162 offset:8800
	global_load_dwordx4 v[62:65], v[158:159], off
	v_lshl_add_u64 v[158:159], v[158:159], 0, s[72:73]
	s_waitcnt vmcnt(23)
	s_waitcnt lgkmcnt(5)
	v_mfma_f32_32x32x16_f16 v[2:17], v[122:125], v[58:61], v[2:17]
	s_waitcnt lgkmcnt(4)
	v_mfma_f32_32x32x16_f16 v[18:33], v[126:129], v[58:61], v[18:33]
	ds_read_b128 v[122:125], v162 offset:128
	ds_read_b128 v[126:129], v162 offset:8832
	global_load_dwordx4 v[58:61], v[158:159], off
	v_lshl_add_u64 v[158:159], v[158:159], 0, s[72:73]
	s_waitcnt vmcnt(23)
	s_waitcnt lgkmcnt(5)
	v_mfma_f32_32x32x16_f16 v[2:17], v[130:133], v[54:57], v[2:17]
	s_waitcnt lgkmcnt(4)
	v_mfma_f32_32x32x16_f16 v[18:33], v[134:137], v[54:57], v[18:33]
	ds_read_b128 v[130:133], v162 offset:160
	ds_read_b128 v[134:137], v162 offset:8864
	global_load_dwordx4 v[54:57], v[158:159], off
	v_lshl_add_u64 v[158:159], v[158:159], 0, s[72:73]
	s_waitcnt vmcnt(23)
	s_waitcnt lgkmcnt(5)
	v_mfma_f32_32x32x16_f16 v[2:17], v[114:117], v[50:53], v[2:17]
	s_waitcnt lgkmcnt(4)
	v_mfma_f32_32x32x16_f16 v[18:33], v[118:121], v[50:53], v[18:33]
	ds_read_b128 v[114:117], v162 offset:192
	ds_read_b128 v[118:121], v162 offset:8896
	global_load_dwordx4 v[50:53], v[158:159], off
	v_lshl_add_u64 v[158:159], v[158:159], 0, s[72:73]
	s_waitcnt vmcnt(23)
	s_waitcnt lgkmcnt(5)
	v_mfma_f32_32x32x16_f16 v[2:17], v[122:125], v[46:49], v[2:17]
	s_waitcnt lgkmcnt(4)
	v_mfma_f32_32x32x16_f16 v[18:33], v[126:129], v[46:49], v[18:33]
	ds_read_b128 v[122:125], v162 offset:224
	ds_read_b128 v[126:129], v162 offset:8928
	global_load_dwordx4 v[46:49], v[158:159], off
	v_lshl_add_u64 v[158:159], v[158:159], 0, s[72:73]
	s_waitcnt vmcnt(23)
	s_waitcnt lgkmcnt(5)
	v_mfma_f32_32x32x16_f16 v[2:17], v[130:133], v[42:45], v[2:17]
	s_waitcnt lgkmcnt(4)
	v_mfma_f32_32x32x16_f16 v[18:33], v[134:137], v[42:45], v[18:33]
	global_load_dwordx4 v[42:45], v[158:159], off
	v_lshl_add_u64 v[158:159], v[158:159], 0, s[72:73]
	s_waitcnt vmcnt(23)
	s_waitcnt lgkmcnt(3)
	v_mfma_f32_32x32x16_f16 v[2:17], v[114:117], v[38:41], v[2:17]
	s_waitcnt lgkmcnt(2)
	v_mfma_f32_32x32x16_f16 v[18:33], v[118:121], v[38:41], v[18:33]
	global_load_dwordx4 v[38:41], v[158:159], off
	v_lshl_add_u64 v[158:159], v[158:159], 0, s[72:73]
	s_waitcnt vmcnt(23)
	s_waitcnt lgkmcnt(1)
	v_mfma_f32_32x32x16_f16 v[2:17], v[122:125], v[34:37], v[2:17]
	s_waitcnt lgkmcnt(0)
	v_mfma_f32_32x32x16_f16 v[18:33], v[126:129], v[34:37], v[18:33]
	global_load_dwordx4 v[34:37], v[158:159], off
	v_lshl_add_u64 v[158:159], v[158:159], 0, s[72:73]
	s_waitcnt lgkmcnt(0)
	s_barrier
	ds_read_b128 v[114:117], v162 offset:17408
	ds_read_b128 v[118:121], v162 offset:26112
	ds_read_b128 v[122:125], v162 offset:17440
	ds_read_b128 v[126:129], v162 offset:26144
	ds_read_b128 v[130:133], v162 offset:17472
	ds_read_b128 v[134:137], v162 offset:26176
	s_waitcnt vmcnt(23)
	s_waitcnt lgkmcnt(5)
	v_mfma_f32_32x32x16_f16 v[2:17], v[114:117], v[94:97], v[2:17]
	s_waitcnt lgkmcnt(4)
	v_mfma_f32_32x32x16_f16 v[18:33], v[118:121], v[94:97], v[18:33]
	ds_read_b128 v[114:117], v162 offset:17504
	ds_read_b128 v[118:121], v162 offset:26208
	global_load_dwordx4 v[94:97], v[158:159], off
	v_lshl_add_u64 v[158:159], v[158:159], 0, s[72:73]
	s_waitcnt vmcnt(23)
	s_waitcnt lgkmcnt(5)
	v_mfma_f32_32x32x16_f16 v[2:17], v[122:125], v[98:101], v[2:17]
	s_waitcnt lgkmcnt(4)
	v_mfma_f32_32x32x16_f16 v[18:33], v[126:129], v[98:101], v[18:33]
	ds_read_b128 v[122:125], v162 offset:17536
	ds_read_b128 v[126:129], v162 offset:26240
	global_load_dwordx4 v[98:101], v[158:159], off
	v_lshl_add_u64 v[158:159], v[158:159], 0, s[72:73]
	s_waitcnt vmcnt(23)
	s_waitcnt lgkmcnt(5)
	v_mfma_f32_32x32x16_f16 v[2:17], v[130:133], v[102:105], v[2:17]
	s_waitcnt lgkmcnt(4)
	v_mfma_f32_32x32x16_f16 v[18:33], v[134:137], v[102:105], v[18:33]
	ds_read_b128 v[130:133], v162 offset:17568
	ds_read_b128 v[134:137], v162 offset:26272
	global_load_dwordx4 v[102:105], v[158:159], off
	v_lshl_add_u64 v[158:159], v[158:159], 0, s[72:73]
	s_waitcnt vmcnt(23)
	s_waitcnt lgkmcnt(5)
	v_mfma_f32_32x32x16_f16 v[2:17], v[114:117], v[106:109], v[2:17]
	s_waitcnt lgkmcnt(4)
	v_mfma_f32_32x32x16_f16 v[18:33], v[118:121], v[106:109], v[18:33]
	ds_read_b128 v[114:117], v162 offset:17600
	ds_read_b128 v[118:121], v162 offset:26304
	global_load_dwordx4 v[106:109], v[158:159], off
	v_lshl_add_u64 v[158:159], v[158:159], 0, s[72:73]
	s_waitcnt vmcnt(23)
	s_waitcnt lgkmcnt(5)
	v_mfma_f32_32x32x16_f16 v[2:17], v[122:125], v[142:145], v[2:17]
	s_waitcnt lgkmcnt(4)
	v_mfma_f32_32x32x16_f16 v[18:33], v[126:129], v[142:145], v[18:33]
	ds_read_b128 v[122:125], v162 offset:17632
	ds_read_b128 v[126:129], v162 offset:26336
	global_load_dwordx4 v[142:145], v[158:159], off
	v_lshl_add_u64 v[158:159], v[158:159], 0, s[72:73]
	s_waitcnt vmcnt(23)
	s_waitcnt lgkmcnt(5)
	v_mfma_f32_32x32x16_f16 v[2:17], v[130:133], v[146:149], v[2:17]
	s_waitcnt lgkmcnt(4)
	v_mfma_f32_32x32x16_f16 v[18:33], v[134:137], v[146:149], v[18:33]
	global_load_dwordx4 v[146:149], v[158:159], off
	v_lshl_add_u64 v[158:159], v[158:159], 0, s[72:73]
	s_waitcnt vmcnt(23)
	s_waitcnt lgkmcnt(3)
	v_mfma_f32_32x32x16_f16 v[2:17], v[114:117], v[150:153], v[2:17]
	s_waitcnt lgkmcnt(2)
	v_mfma_f32_32x32x16_f16 v[18:33], v[118:121], v[150:153], v[18:33]
	global_load_dwordx4 v[150:153], v[158:159], off
	v_lshl_add_u64 v[158:159], v[158:159], 0, s[72:73]
	s_waitcnt vmcnt(23)
	s_waitcnt lgkmcnt(1)
	v_mfma_f32_32x32x16_f16 v[2:17], v[122:125], v[154:157], v[2:17]
	s_waitcnt lgkmcnt(0)
	v_mfma_f32_32x32x16_f16 v[18:33], v[126:129], v[154:157], v[18:33]
	global_load_dwordx4 v[154:157], v[158:159], off
	v_lshl_add_u64 v[158:159], v[158:159], 0, s[72:73]
	s_waitcnt lgkmcnt(0)
	s_barrier
	ds_read_b128 v[114:117], v162 offset:34816
	ds_read_b128 v[118:121], v162 offset:43520
	ds_read_b128 v[122:125], v162 offset:34848
	ds_read_b128 v[126:129], v162 offset:43552
	ds_read_b128 v[130:133], v162 offset:34880
	ds_read_b128 v[134:137], v162 offset:43584
	s_waitcnt vmcnt(23)
	s_waitcnt lgkmcnt(5)
	v_mfma_f32_32x32x16_f16 v[2:17], v[114:117], v[110:113], v[2:17]
	s_waitcnt lgkmcnt(4)
	v_mfma_f32_32x32x16_f16 v[18:33], v[118:121], v[110:113], v[18:33]
	ds_read_b128 v[114:117], v162 offset:34912
	ds_read_b128 v[118:121], v162 offset:43616
	global_load_dwordx4 v[110:113], v[158:159], off
	v_lshl_add_u64 v[158:159], v[158:159], 0, s[72:73]
	s_waitcnt vmcnt(23)
	s_waitcnt lgkmcnt(5)
	v_mfma_f32_32x32x16_f16 v[2:17], v[122:125], v[90:93], v[2:17]
	s_waitcnt lgkmcnt(4)
	v_mfma_f32_32x32x16_f16 v[18:33], v[126:129], v[90:93], v[18:33]
	ds_read_b128 v[122:125], v162 offset:34944
	ds_read_b128 v[126:129], v162 offset:43648
	global_load_dwordx4 v[90:93], v[158:159], off
	v_lshl_add_u64 v[158:159], v[158:159], 0, s[72:73]
	s_waitcnt vmcnt(23)
	s_waitcnt lgkmcnt(5)
	v_mfma_f32_32x32x16_f16 v[2:17], v[130:133], v[86:89], v[2:17]
	s_waitcnt lgkmcnt(4)
	v_mfma_f32_32x32x16_f16 v[18:33], v[134:137], v[86:89], v[18:33]
	ds_read_b128 v[130:133], v162 offset:34976
	ds_read_b128 v[134:137], v162 offset:43680
	global_load_dwordx4 v[86:89], v[158:159], off
	v_lshl_add_u64 v[158:159], v[158:159], 0, s[72:73]
	s_waitcnt vmcnt(23)
	s_waitcnt lgkmcnt(5)
	v_mfma_f32_32x32x16_f16 v[2:17], v[114:117], v[82:85], v[2:17]
	s_waitcnt lgkmcnt(4)
	v_mfma_f32_32x32x16_f16 v[18:33], v[118:121], v[82:85], v[18:33]
	ds_read_b128 v[114:117], v162 offset:35008
	ds_read_b128 v[118:121], v162 offset:43712
	global_load_dwordx4 v[82:85], v[158:159], off
	v_lshl_add_u64 v[158:159], v[158:159], 0, s[72:73]
	s_waitcnt vmcnt(23)
	s_waitcnt lgkmcnt(5)
	v_mfma_f32_32x32x16_f16 v[2:17], v[122:125], v[78:81], v[2:17]
	s_waitcnt lgkmcnt(4)
	v_mfma_f32_32x32x16_f16 v[18:33], v[126:129], v[78:81], v[18:33]
	ds_read_b128 v[122:125], v162 offset:35040
	ds_read_b128 v[126:129], v162 offset:43744
	global_load_dwordx4 v[78:81], v[158:159], off
	v_lshl_add_u64 v[158:159], v[158:159], 0, s[72:73]
	s_waitcnt vmcnt(23)
	s_waitcnt lgkmcnt(5)
	v_mfma_f32_32x32x16_f16 v[2:17], v[130:133], v[74:77], v[2:17]
	s_waitcnt lgkmcnt(4)
	v_mfma_f32_32x32x16_f16 v[18:33], v[134:137], v[74:77], v[18:33]
	global_load_dwordx4 v[74:77], v[158:159], off
	v_lshl_add_u64 v[158:159], v[158:159], 0, s[72:73]
	s_waitcnt vmcnt(23)
	s_waitcnt lgkmcnt(3)
	v_mfma_f32_32x32x16_f16 v[2:17], v[114:117], v[70:73], v[2:17]
	s_waitcnt lgkmcnt(2)
	v_mfma_f32_32x32x16_f16 v[18:33], v[118:121], v[70:73], v[18:33]
	global_load_dwordx4 v[70:73], v[158:159], off
	v_lshl_add_u64 v[158:159], v[158:159], 0, s[72:73]
	s_waitcnt vmcnt(23)
	s_waitcnt lgkmcnt(1)
	v_mfma_f32_32x32x16_f16 v[2:17], v[122:125], v[66:69], v[2:17]
	s_waitcnt lgkmcnt(0)
	v_mfma_f32_32x32x16_f16 v[18:33], v[126:129], v[66:69], v[18:33]
	global_load_dwordx4 v[66:69], v[158:159], off
	v_lshl_add_u64 v[158:159], v[158:159], 0, s[72:73]
	s_waitcnt lgkmcnt(0)
	s_barrier
	ds_read_b128 v[114:117], v162 offset:52224
	ds_read_b128 v[118:121], v162 offset:60928
	ds_read_b128 v[122:125], v162 offset:52256
	ds_read_b128 v[126:129], v162 offset:60960
	ds_read_b128 v[130:133], v162 offset:52288
	ds_read_b128 v[134:137], v162 offset:60992
	s_waitcnt vmcnt(23)
	s_waitcnt lgkmcnt(5)
	v_mfma_f32_32x32x16_f16 v[2:17], v[114:117], v[62:65], v[2:17]
	s_waitcnt lgkmcnt(4)
	v_mfma_f32_32x32x16_f16 v[18:33], v[118:121], v[62:65], v[18:33]
	ds_read_b128 v[114:117], v162 offset:52320
	ds_read_b128 v[118:121], v162 offset:61024
	global_load_dwordx4 v[62:65], v[158:159], off
	v_lshl_add_u64 v[158:159], v[158:159], 0, s[72:73]
	s_waitcnt vmcnt(23)
	s_waitcnt lgkmcnt(5)
	v_mfma_f32_32x32x16_f16 v[2:17], v[122:125], v[58:61], v[2:17]
	s_waitcnt lgkmcnt(4)
	v_mfma_f32_32x32x16_f16 v[18:33], v[126:129], v[58:61], v[18:33]
	ds_read_b128 v[122:125], v162 offset:52352
	ds_read_b128 v[126:129], v162 offset:61056
	global_load_dwordx4 v[58:61], v[158:159], off
	v_lshl_add_u64 v[158:159], v[158:159], 0, s[72:73]
	s_waitcnt vmcnt(23)
	s_waitcnt lgkmcnt(5)
	v_mfma_f32_32x32x16_f16 v[2:17], v[130:133], v[54:57], v[2:17]
	s_waitcnt lgkmcnt(4)
	v_mfma_f32_32x32x16_f16 v[18:33], v[134:137], v[54:57], v[18:33]
	ds_read_b128 v[130:133], v162 offset:52384
	ds_read_b128 v[134:137], v162 offset:61088
	global_load_dwordx4 v[54:57], v[158:159], off
	v_lshl_add_u64 v[158:159], v[158:159], 0, s[72:73]
	s_waitcnt vmcnt(23)
	s_waitcnt lgkmcnt(5)
	v_mfma_f32_32x32x16_f16 v[2:17], v[114:117], v[50:53], v[2:17]
	s_waitcnt lgkmcnt(4)
	v_mfma_f32_32x32x16_f16 v[18:33], v[118:121], v[50:53], v[18:33]
	ds_read_b128 v[114:117], v162 offset:52416
	ds_read_b128 v[118:121], v162 offset:61120
	global_load_dwordx4 v[50:53], v[158:159], off
	v_lshl_add_u64 v[158:159], v[158:159], 0, s[72:73]
	s_waitcnt vmcnt(23)
	s_waitcnt lgkmcnt(5)
	v_mfma_f32_32x32x16_f16 v[2:17], v[122:125], v[46:49], v[2:17]
	s_waitcnt lgkmcnt(4)
	v_mfma_f32_32x32x16_f16 v[18:33], v[126:129], v[46:49], v[18:33]
	ds_read_b128 v[122:125], v162 offset:52448
	ds_read_b128 v[126:129], v162 offset:61152
	global_load_dwordx4 v[46:49], v[158:159], off
	v_lshl_add_u64 v[158:159], v[158:159], 0, s[72:73]
	s_waitcnt vmcnt(23)
	s_waitcnt lgkmcnt(5)
	v_mfma_f32_32x32x16_f16 v[2:17], v[130:133], v[42:45], v[2:17]
	s_waitcnt lgkmcnt(4)
	v_mfma_f32_32x32x16_f16 v[18:33], v[134:137], v[42:45], v[18:33]
	global_load_dwordx4 v[42:45], v[158:159], off
	v_lshl_add_u64 v[158:159], v[158:159], 0, s[72:73]
	s_waitcnt vmcnt(23)
	s_waitcnt lgkmcnt(3)
	v_mfma_f32_32x32x16_f16 v[2:17], v[114:117], v[38:41], v[2:17]
	s_waitcnt lgkmcnt(2)
	v_mfma_f32_32x32x16_f16 v[18:33], v[118:121], v[38:41], v[18:33]
	global_load_dwordx4 v[38:41], v[158:159], off
	v_lshl_add_u64 v[158:159], v[158:159], 0, s[72:73]
	s_waitcnt vmcnt(23)
	s_waitcnt lgkmcnt(1)
	v_mfma_f32_32x32x16_f16 v[2:17], v[122:125], v[34:37], v[2:17]
	s_waitcnt lgkmcnt(0)
	v_mfma_f32_32x32x16_f16 v[18:33], v[126:129], v[34:37], v[18:33]
	global_load_dwordx4 v[34:37], v[158:159], off
	v_lshl_add_u64 v[158:159], v[158:159], 0, s[72:73]
	s_waitcnt lgkmcnt(0)
	s_barrier
	ds_read_b128 v[114:117], v162 offset:0
	ds_read_b128 v[118:121], v162 offset:8704
	ds_read_b128 v[122:125], v162 offset:32
	ds_read_b128 v[126:129], v162 offset:8736
	ds_read_b128 v[130:133], v162 offset:64
	ds_read_b128 v[134:137], v162 offset:8768
	s_waitcnt vmcnt(23)
	s_waitcnt lgkmcnt(5)
	v_mfma_f32_32x32x16_f16 v[2:17], v[114:117], v[94:97], v[2:17]
	s_waitcnt lgkmcnt(4)
	v_mfma_f32_32x32x16_f16 v[18:33], v[118:121], v[94:97], v[18:33]
	ds_read_b128 v[114:117], v162 offset:96
	ds_read_b128 v[118:121], v162 offset:8800
	global_load_dwordx4 v[94:97], v[158:159], off
	v_lshl_add_u64 v[158:159], v[158:159], 0, s[72:73]
	s_waitcnt vmcnt(23)
	s_waitcnt lgkmcnt(5)
	v_mfma_f32_32x32x16_f16 v[2:17], v[122:125], v[98:101], v[2:17]
	s_waitcnt lgkmcnt(4)
	v_mfma_f32_32x32x16_f16 v[18:33], v[126:129], v[98:101], v[18:33]
	ds_read_b128 v[122:125], v162 offset:128
	ds_read_b128 v[126:129], v162 offset:8832
	global_load_dwordx4 v[98:101], v[158:159], off
	v_lshl_add_u64 v[158:159], v[158:159], 0, s[72:73]
	s_waitcnt vmcnt(23)
	s_waitcnt lgkmcnt(5)
	v_mfma_f32_32x32x16_f16 v[2:17], v[130:133], v[102:105], v[2:17]
	s_waitcnt lgkmcnt(4)
	v_mfma_f32_32x32x16_f16 v[18:33], v[134:137], v[102:105], v[18:33]
	ds_read_b128 v[130:133], v162 offset:160
	ds_read_b128 v[134:137], v162 offset:8864
	global_load_dwordx4 v[102:105], v[158:159], off
	v_lshl_add_u64 v[158:159], v[158:159], 0, s[72:73]
	s_waitcnt vmcnt(23)
	s_waitcnt lgkmcnt(5)
	v_mfma_f32_32x32x16_f16 v[2:17], v[114:117], v[106:109], v[2:17]
	s_waitcnt lgkmcnt(4)
	v_mfma_f32_32x32x16_f16 v[18:33], v[118:121], v[106:109], v[18:33]
	ds_read_b128 v[114:117], v162 offset:192
	ds_read_b128 v[118:121], v162 offset:8896
	global_load_dwordx4 v[106:109], v[158:159], off
	v_lshl_add_u64 v[158:159], v[158:159], 0, s[72:73]
	s_waitcnt vmcnt(23)
	s_waitcnt lgkmcnt(5)
	v_mfma_f32_32x32x16_f16 v[2:17], v[122:125], v[142:145], v[2:17]
	s_waitcnt lgkmcnt(4)
	v_mfma_f32_32x32x16_f16 v[18:33], v[126:129], v[142:145], v[18:33]
	ds_read_b128 v[122:125], v162 offset:224
	ds_read_b128 v[126:129], v162 offset:8928
	global_load_dwordx4 v[142:145], v[158:159], off
	v_lshl_add_u64 v[158:159], v[158:159], 0, s[72:73]
	s_waitcnt vmcnt(23)
	s_waitcnt lgkmcnt(5)
	v_mfma_f32_32x32x16_f16 v[2:17], v[130:133], v[146:149], v[2:17]
	s_waitcnt lgkmcnt(4)
	v_mfma_f32_32x32x16_f16 v[18:33], v[134:137], v[146:149], v[18:33]
	global_load_dwordx4 v[146:149], v[158:159], off
	v_lshl_add_u64 v[158:159], v[158:159], 0, s[72:73]
	s_waitcnt vmcnt(23)
	s_waitcnt lgkmcnt(3)
	v_mfma_f32_32x32x16_f16 v[2:17], v[114:117], v[150:153], v[2:17]
	s_waitcnt lgkmcnt(2)
	v_mfma_f32_32x32x16_f16 v[18:33], v[118:121], v[150:153], v[18:33]
	global_load_dwordx4 v[150:153], v[158:159], off
	v_lshl_add_u64 v[158:159], v[158:159], 0, s[72:73]
	s_waitcnt vmcnt(23)
	s_waitcnt lgkmcnt(1)
	v_mfma_f32_32x32x16_f16 v[2:17], v[122:125], v[154:157], v[2:17]
	s_waitcnt lgkmcnt(0)
	v_mfma_f32_32x32x16_f16 v[18:33], v[126:129], v[154:157], v[18:33]
	global_load_dwordx4 v[154:157], v[158:159], off
	v_lshl_add_u64 v[158:159], v[158:159], 0, s[72:73]
	s_waitcnt lgkmcnt(0)
	s_barrier
	ds_read_b128 v[114:117], v162 offset:17408
	ds_read_b128 v[118:121], v162 offset:26112
	ds_read_b128 v[122:125], v162 offset:17440
	ds_read_b128 v[126:129], v162 offset:26144
	ds_read_b128 v[130:133], v162 offset:17472
	ds_read_b128 v[134:137], v162 offset:26176
	s_waitcnt vmcnt(23)
	s_waitcnt lgkmcnt(5)
	v_mfma_f32_32x32x16_f16 v[2:17], v[114:117], v[110:113], v[2:17]
	s_waitcnt lgkmcnt(4)
	v_mfma_f32_32x32x16_f16 v[18:33], v[118:121], v[110:113], v[18:33]
	ds_read_b128 v[114:117], v162 offset:17504
	ds_read_b128 v[118:121], v162 offset:26208
	s_waitcnt vmcnt(22)
	s_waitcnt lgkmcnt(5)
	v_mfma_f32_32x32x16_f16 v[2:17], v[122:125], v[90:93], v[2:17]
	s_waitcnt lgkmcnt(4)
	v_mfma_f32_32x32x16_f16 v[18:33], v[126:129], v[90:93], v[18:33]
	ds_read_b128 v[122:125], v162 offset:17536
	ds_read_b128 v[126:129], v162 offset:26240
	s_waitcnt vmcnt(21)
	s_waitcnt lgkmcnt(5)
	v_mfma_f32_32x32x16_f16 v[2:17], v[130:133], v[86:89], v[2:17]
	s_waitcnt lgkmcnt(4)
	v_mfma_f32_32x32x16_f16 v[18:33], v[134:137], v[86:89], v[18:33]
	ds_read_b128 v[130:133], v162 offset:17568
	ds_read_b128 v[134:137], v162 offset:26272
	s_waitcnt vmcnt(20)
	s_waitcnt lgkmcnt(5)
	v_mfma_f32_32x32x16_f16 v[2:17], v[114:117], v[82:85], v[2:17]
	s_waitcnt lgkmcnt(4)
	v_mfma_f32_32x32x16_f16 v[18:33], v[118:121], v[82:85], v[18:33]
	ds_read_b128 v[114:117], v162 offset:17600
	ds_read_b128 v[118:121], v162 offset:26304
	s_waitcnt vmcnt(19)
	s_waitcnt lgkmcnt(5)
	v_mfma_f32_32x32x16_f16 v[2:17], v[122:125], v[78:81], v[2:17]
	s_waitcnt lgkmcnt(4)
	v_mfma_f32_32x32x16_f16 v[18:33], v[126:129], v[78:81], v[18:33]
	ds_read_b128 v[122:125], v162 offset:17632
	ds_read_b128 v[126:129], v162 offset:26336
	s_waitcnt vmcnt(18)
	s_waitcnt lgkmcnt(5)
	v_mfma_f32_32x32x16_f16 v[2:17], v[130:133], v[74:77], v[2:17]
	s_waitcnt lgkmcnt(4)
	v_mfma_f32_32x32x16_f16 v[18:33], v[134:137], v[74:77], v[18:33]
	s_waitcnt vmcnt(17)
	s_waitcnt lgkmcnt(3)
	v_mfma_f32_32x32x16_f16 v[2:17], v[114:117], v[70:73], v[2:17]
	s_waitcnt lgkmcnt(2)
	v_mfma_f32_32x32x16_f16 v[18:33], v[118:121], v[70:73], v[18:33]
	s_waitcnt vmcnt(16)
	s_waitcnt lgkmcnt(1)
	v_mfma_f32_32x32x16_f16 v[2:17], v[122:125], v[66:69], v[2:17]
	s_waitcnt lgkmcnt(0)
	v_mfma_f32_32x32x16_f16 v[18:33], v[126:129], v[66:69], v[18:33]
	s_waitcnt lgkmcnt(0)
	s_barrier
	ds_read_b128 v[114:117], v162 offset:34816
	ds_read_b128 v[118:121], v162 offset:43520
	ds_read_b128 v[122:125], v162 offset:34848
	ds_read_b128 v[126:129], v162 offset:43552
	ds_read_b128 v[130:133], v162 offset:34880
	ds_read_b128 v[134:137], v162 offset:43584
	s_waitcnt vmcnt(15)
	s_waitcnt lgkmcnt(5)
	v_mfma_f32_32x32x16_f16 v[2:17], v[114:117], v[62:65], v[2:17]
	s_waitcnt lgkmcnt(4)
	v_mfma_f32_32x32x16_f16 v[18:33], v[118:121], v[62:65], v[18:33]
	ds_read_b128 v[114:117], v162 offset:34912
	ds_read_b128 v[118:121], v162 offset:43616
	s_waitcnt vmcnt(14)
	s_waitcnt lgkmcnt(5)
	v_mfma_f32_32x32x16_f16 v[2:17], v[122:125], v[58:61], v[2:17]
	s_waitcnt lgkmcnt(4)
	v_mfma_f32_32x32x16_f16 v[18:33], v[126:129], v[58:61], v[18:33]
	ds_read_b128 v[122:125], v162 offset:34944
	ds_read_b128 v[126:129], v162 offset:43648
	s_waitcnt vmcnt(13)
	s_waitcnt lgkmcnt(5)
	v_mfma_f32_32x32x16_f16 v[2:17], v[130:133], v[54:57], v[2:17]
	s_waitcnt lgkmcnt(4)
	v_mfma_f32_32x32x16_f16 v[18:33], v[134:137], v[54:57], v[18:33]
	ds_read_b128 v[130:133], v162 offset:34976
	ds_read_b128 v[134:137], v162 offset:43680
	s_waitcnt vmcnt(12)
	s_waitcnt lgkmcnt(5)
	v_mfma_f32_32x32x16_f16 v[2:17], v[114:117], v[50:53], v[2:17]
	s_waitcnt lgkmcnt(4)
	v_mfma_f32_32x32x16_f16 v[18:33], v[118:121], v[50:53], v[18:33]
	ds_read_b128 v[114:117], v162 offset:35008
	ds_read_b128 v[118:121], v162 offset:43712
	s_waitcnt vmcnt(11)
	s_waitcnt lgkmcnt(5)
	v_mfma_f32_32x32x16_f16 v[2:17], v[122:125], v[46:49], v[2:17]
	s_waitcnt lgkmcnt(4)
	v_mfma_f32_32x32x16_f16 v[18:33], v[126:129], v[46:49], v[18:33]
	ds_read_b128 v[122:125], v162 offset:35040
	ds_read_b128 v[126:129], v162 offset:43744
	s_waitcnt vmcnt(10)
	s_waitcnt lgkmcnt(5)
	v_mfma_f32_32x32x16_f16 v[2:17], v[130:133], v[42:45], v[2:17]
	s_waitcnt lgkmcnt(4)
	v_mfma_f32_32x32x16_f16 v[18:33], v[134:137], v[42:45], v[18:33]
	s_waitcnt vmcnt(9)
	s_waitcnt lgkmcnt(3)
	v_mfma_f32_32x32x16_f16 v[2:17], v[114:117], v[38:41], v[2:17]
	s_waitcnt lgkmcnt(2)
	v_mfma_f32_32x32x16_f16 v[18:33], v[118:121], v[38:41], v[18:33]
	s_waitcnt vmcnt(8)
	s_waitcnt lgkmcnt(1)
	v_mfma_f32_32x32x16_f16 v[2:17], v[122:125], v[34:37], v[2:17]
	s_waitcnt lgkmcnt(0)
	v_mfma_f32_32x32x16_f16 v[18:33], v[126:129], v[34:37], v[18:33]
	s_waitcnt lgkmcnt(0)
	s_barrier
	ds_read_b128 v[114:117], v162 offset:52224
	ds_read_b128 v[118:121], v162 offset:60928
	ds_read_b128 v[122:125], v162 offset:52256
	ds_read_b128 v[126:129], v162 offset:60960
	ds_read_b128 v[130:133], v162 offset:52288
	ds_read_b128 v[134:137], v162 offset:60992
	s_waitcnt vmcnt(7)
	s_waitcnt lgkmcnt(5)
	v_mfma_f32_32x32x16_f16 v[2:17], v[114:117], v[94:97], v[2:17]
	s_waitcnt lgkmcnt(4)
	v_mfma_f32_32x32x16_f16 v[18:33], v[118:121], v[94:97], v[18:33]
	ds_read_b128 v[114:117], v162 offset:52320
	ds_read_b128 v[118:121], v162 offset:61024
	s_waitcnt vmcnt(6)
	s_waitcnt lgkmcnt(5)
	v_mfma_f32_32x32x16_f16 v[2:17], v[122:125], v[98:101], v[2:17]
	s_waitcnt lgkmcnt(4)
	v_mfma_f32_32x32x16_f16 v[18:33], v[126:129], v[98:101], v[18:33]
	ds_read_b128 v[122:125], v162 offset:52352
	ds_read_b128 v[126:129], v162 offset:61056
	s_waitcnt vmcnt(5)
	s_waitcnt lgkmcnt(5)
	v_mfma_f32_32x32x16_f16 v[2:17], v[130:133], v[102:105], v[2:17]
	s_waitcnt lgkmcnt(4)
	v_mfma_f32_32x32x16_f16 v[18:33], v[134:137], v[102:105], v[18:33]
	ds_read_b128 v[130:133], v162 offset:52384
	ds_read_b128 v[134:137], v162 offset:61088
	s_waitcnt vmcnt(4)
	s_waitcnt lgkmcnt(5)
	v_mfma_f32_32x32x16_f16 v[2:17], v[114:117], v[106:109], v[2:17]
	s_waitcnt lgkmcnt(4)
	v_mfma_f32_32x32x16_f16 v[18:33], v[118:121], v[106:109], v[18:33]
	ds_read_b128 v[114:117], v162 offset:52416
	ds_read_b128 v[118:121], v162 offset:61120
	s_waitcnt vmcnt(3)
	s_waitcnt lgkmcnt(5)
	v_mfma_f32_32x32x16_f16 v[2:17], v[122:125], v[142:145], v[2:17]
	s_waitcnt lgkmcnt(4)
	v_mfma_f32_32x32x16_f16 v[18:33], v[126:129], v[142:145], v[18:33]
	ds_read_b128 v[122:125], v162 offset:52448
	ds_read_b128 v[126:129], v162 offset:61152
	s_waitcnt vmcnt(2)
	s_waitcnt lgkmcnt(5)
	v_mfma_f32_32x32x16_f16 v[2:17], v[130:133], v[146:149], v[2:17]
	s_waitcnt lgkmcnt(4)
	v_mfma_f32_32x32x16_f16 v[18:33], v[134:137], v[146:149], v[18:33]
	s_waitcnt vmcnt(1)
	s_waitcnt lgkmcnt(3)
	v_mfma_f32_32x32x16_f16 v[2:17], v[114:117], v[150:153], v[2:17]
	s_waitcnt lgkmcnt(2)
	v_mfma_f32_32x32x16_f16 v[18:33], v[118:121], v[150:153], v[18:33]
	s_waitcnt vmcnt(0)
	s_waitcnt lgkmcnt(1)
	v_mfma_f32_32x32x16_f16 v[2:17], v[122:125], v[154:157], v[2:17]
	s_waitcnt lgkmcnt(0)
	v_mfma_f32_32x32x16_f16 v[18:33], v[126:129], v[154:157], v[18:33]
	s_waitcnt lgkmcnt(0)
	s_barrier
	s_mov_b32 s2, 0x3d800000
	v_mul_u32_u24_e32 v1, 0x420, v1
	v_or_b32_e32 v34, v161, v160
	v_lshlrev_b32_e32 v34, 1, v34
	v_lshl_add_u32 v1, v1, 1, v34
	s_nop 7
	s_nop 7
	v_fma_mixlo_f16 v2, v2, s2, 0
	ds_write_b16 v1, v2
	v_fma_mixlo_f16 v2, v18, s2, 0
	ds_write_b16 v1, v2 offset:16896
	v_fma_mixlo_f16 v2, v3, s2, 0
	ds_write_b16 v1, v2 offset:528
	v_fma_mixlo_f16 v2, v19, s2, 0
	ds_write_b16 v1, v2 offset:17424
	v_fma_mixlo_f16 v2, v4, s2, 0
	ds_write_b16 v1, v2 offset:1056
	v_fma_mixlo_f16 v2, v20, s2, 0
	ds_write_b16 v1, v2 offset:17952
	v_fma_mixlo_f16 v2, v5, s2, 0
	ds_write_b16 v1, v2 offset:1584
	v_fma_mixlo_f16 v2, v21, s2, 0
	ds_write_b16 v1, v2 offset:18480
	v_fma_mixlo_f16 v2, v6, s2, 0
	ds_write_b16 v1, v2 offset:4224
	v_fma_mixlo_f16 v2, v22, s2, 0
	ds_write_b16 v1, v2 offset:21120
	v_fma_mixlo_f16 v2, v7, s2, 0
	ds_write_b16 v1, v2 offset:4752
	v_fma_mixlo_f16 v2, v23, s2, 0
	ds_write_b16 v1, v2 offset:21648
	v_fma_mixlo_f16 v2, v8, s2, 0
	ds_write_b16 v1, v2 offset:5280
	v_fma_mixlo_f16 v2, v24, s2, 0
	ds_write_b16 v1, v2 offset:22176
	v_fma_mixlo_f16 v2, v9, s2, 0
	ds_write_b16 v1, v2 offset:5808
	v_fma_mixlo_f16 v2, v25, s2, 0
	ds_write_b16 v1, v2 offset:22704
	v_fma_mixlo_f16 v2, v10, s2, 0
	ds_write_b16 v1, v2 offset:8448
	v_fma_mixlo_f16 v2, v26, s2, 0
	ds_write_b16 v1, v2 offset:25344
	v_fma_mixlo_f16 v2, v11, s2, 0
	ds_write_b16 v1, v2 offset:8976
	v_fma_mixlo_f16 v2, v27, s2, 0
	ds_write_b16 v1, v2 offset:25872
	v_fma_mixlo_f16 v2, v12, s2, 0
	ds_write_b16 v1, v2 offset:9504
	v_fma_mixlo_f16 v2, v28, s2, 0
	ds_write_b16 v1, v2 offset:26400
	v_fma_mixlo_f16 v2, v13, s2, 0
	ds_write_b16 v1, v2 offset:10032
	v_fma_mixlo_f16 v2, v29, s2, 0
	ds_write_b16 v1, v2 offset:26928
	v_fma_mixlo_f16 v2, v14, s2, 0
	ds_write_b16 v1, v2 offset:12672
	v_fma_mixlo_f16 v2, v30, s2, 0
	ds_write_b16 v1, v2 offset:29568
	v_fma_mixlo_f16 v2, v15, s2, 0
	ds_write_b16 v1, v2 offset:13200
	v_fma_mixlo_f16 v2, v31, s2, 0
	ds_write_b16 v1, v2 offset:30096
	v_fma_mixlo_f16 v2, v16, s2, 0
	ds_write_b16 v1, v2 offset:13728
	v_fma_mixlo_f16 v2, v32, s2, 0
	ds_write_b16 v1, v2 offset:30624
	v_fma_mixlo_f16 v2, v17, s2, 0
	ds_write_b16 v1, v2 offset:14256
	v_fma_mixlo_f16 v2, v33, s2, 0
	ds_write_b16 v1, v2 offset:31152
	v_lshrrev_b32_e32 v1, 3, v0
	v_lshlrev_b32_e32 v0, 4, v0
	v_and_b32_e32 v4, 0x70, v0
	s_movk_i32 s2, 0x210
	v_mad_u32_u24 v12, v1, s2, v4
	s_ashr_i32 s2, s8, 31
	s_waitcnt lgkmcnt(0)
	s_barrier
	v_or_b32_e32 v6, s8, v1
	v_mov_b32_e32 v7, s2
	v_mov_b32_e32 v5, 0
	ds_read_b128 v[0:3], v12
	v_lshl_add_u64 v[4:5], s[16:17], 0, v[4:5]
	v_lshlrev_b64 v[6:7], 7, v[6:7]
	v_lshl_add_u64 v[8:9], v[4:5], 0, v[6:7]
	ds_read_b128 v[4:7], v12 offset:128
	s_mov_b32 s2, 0x200000
	s_waitcnt lgkmcnt(1)
	global_store_dwordx4 v[8:9], v[0:3], off
	s_nop 1
	v_add_co_u32_e32 v0, vcc, s2, v8
	s_nop 1
	v_addc_co_u32_e32 v1, vcc, 0, v9, vcc
	s_waitcnt lgkmcnt(0)
	global_store_dwordx4 v[0:1], v[4:7], off
	ds_read_b128 v[0:3], v12 offset:256
	ds_read_b128 v[4:7], v12 offset:384
	v_add_co_u32_e32 v10, vcc, 0x400000, v8
	s_nop 1
	v_addc_co_u32_e32 v11, vcc, 0, v9, vcc
	s_waitcnt lgkmcnt(1)
	global_store_dwordx4 v[10:11], v[0:3], off
	s_nop 1
	v_add_co_u32_e32 v0, vcc, 0x600000, v8
	s_nop 1
	v_addc_co_u32_e32 v1, vcc, 0, v9, vcc
	s_waitcnt lgkmcnt(0)
	global_store_dwordx4 v[0:1], v[4:7], off
	s_andn2_saveexec_b64 s[0:1], s[0:1]
	s_cbranch_execz .LBB1_234
.LBB1_248:
	v_and_b32_e32 v6, 31, v0
	v_bfe_u32 v7, v0, 5, 3
	s_cmp_lt_u32 s8, 0x2000
	s_cselect_b32 s50, s12, s14
	s_cselect_b32 s51, s13, s15
	s_and_b32 s0, s8, 0x1fff
	s_mul_i32 s1, s0, 0x2ee0
	s_add_u32 s50, s50, s1
	s_addc_u32 s51, s51, 0
	s_mov_b32 s52, s50
	s_mov_b32 s53, s51
	s_add_u32 s54, s50, 0x17700
	s_addc_u32 s55, s51, 0
	s_add_u32 s56, s50, 0x2ee00
	s_addc_u32 s57, s51, 0
	s_add_u32 s58, s50, 0x46500
	s_addc_u32 s59, s51, 0
	s_add_u32 s60, s50, 0x5dc00
	s_addc_u32 s61, s51, 0
	s_add_u32 s62, s50, 0x75300
	s_addc_u32 s63, s51, 0
	s_add_u32 s64, s50, 0x8ca00
	s_addc_u32 s65, s51, 0
	s_add_u32 s66, s50, 0xa4100
	s_addc_u32 s67, s51, 0
	v_and_b32_e32 v136, 3, v7
	v_lshl_add_u32 v137, v136, 1, v6
	s_movk_i32 s0, 0x2ee0
	v_mul_lo_u32 v2, v7, s0
	v_lshl_add_u32 v2, v137, 4, v2
	s_movk_i32 s0, 0x110
	v_mul_lo_u32 v3, v7, s0
	v_lshl_add_u32 v138, v137, 3, v3
	v_cmp_le_u32_e64 s[76:77], 32, v137
	v_cmp_gt_u32_e64 s[68:69], 14, v137
	s_not_b64 s[78:79], s[76:77]
	v_mov_b32_e32 v139, 0x0
	v_mov_b32_e32 v140, 0x4300
	v_cndmask_b32_e64 v139, v139, v140, s[76:77]
	v_add_u32_e32 v141, v138, v139
	v_mov_b32_e32 v139, 0x4400
	v_mov_b32_e32 v140, 0x8700
	v_cndmask_b32_e64 v139, v139, v140, s[76:77]
	v_add_u32_e32 v142, v138, v139
	v_mov_b32_e32 v139, 0x8800
	v_mov_b32_e32 v140, 0xcb00
	v_cndmask_b32_e64 v139, v139, v140, s[76:77]
	v_add_u32_e32 v143, v138, v139
	v_mov_b32_e32 v139, 0xcc00
	v_mov_b32_e32 v140, 0xffffff00
	v_cndmask_b32_e64 v139, v139, v140, s[76:77]
	v_add_u32_e32 v144, v138, v139
	s_add_u32 s48, s18, 0x100000
	s_addc_u32 s49, s19, 0
	s_lshl_b32 s0, s10, 12
	v_add_u32_e32 v150, 0xfffffe00, v0
	v_lshl_add_u32 v150, v150, 4, s0
	global_load_dwordx4 v[152:155], v150, s[48:49]
	global_load_dwordx4 v[156:159], v150, s[18:19]
	v_mov_b32_e32 v104, 0
	v_mov_b32_e32 v105, 0
	v_mov_b32_e32 v106, 0
	v_mov_b32_e32 v107, 0
	s_mov_b64 s[70:71], exec
	s_mov_b64 exec, s[76:77]
	global_load_dwordx4 v[104:107], v2, s[52:53] offset:-512 sc1 nt
	s_mov_b64 exec, s[70:71]
	v_mov_b32_e32 v108, 0
	v_mov_b32_e32 v109, 0
	v_mov_b32_e32 v110, 0
	v_mov_b32_e32 v111, 0
	s_mov_b64 s[70:71], exec
	s_mov_b64 exec, s[76:77]
	global_load_dwordx4 v[108:111], v2, s[54:55] offset:-512 sc1 nt
	s_mov_b64 exec, s[70:71]
	v_mov_b32_e32 v112, 0
	v_mov_b32_e32 v113, 0
	v_mov_b32_e32 v114, 0
	v_mov_b32_e32 v115, 0
	s_mov_b64 s[70:71], exec
	s_mov_b64 exec, s[76:77]
	global_load_dwordx4 v[112:115], v2, s[56:57] offset:-512 sc1 nt
	s_mov_b64 exec, s[70:71]
	v_mov_b32_e32 v116, 0
	v_mov_b32_e32 v117, 0
	v_mov_b32_e32 v118, 0
	v_mov_b32_e32 v119, 0
	s_mov_b64 s[70:71], exec
	s_mov_b64 exec, s[76:77]
	global_load_dwordx4 v[116:119], v2, s[58:59] offset:-512 sc1 nt
	s_mov_b64 exec, s[70:71]
	v_mov_b32_e32 v120, 0
	v_mov_b32_e32 v121, 0
	v_mov_b32_e32 v122, 0
	v_mov_b32_e32 v123, 0
	s_mov_b64 s[70:71], exec
	s_mov_b64 exec, s[76:77]
	global_load_dwordx4 v[120:123], v2, s[60:61] offset:-512 sc1 nt
	s_mov_b64 exec, s[70:71]
	v_mov_b32_e32 v124, 0
	v_mov_b32_e32 v125, 0
	v_mov_b32_e32 v126, 0
	v_mov_b32_e32 v127, 0
	s_mov_b64 s[70:71], exec
	s_mov_b64 exec, s[76:77]
	global_load_dwordx4 v[124:127], v2, s[62:63] offset:-512 sc1 nt
	s_mov_b64 exec, s[70:71]
	v_mov_b32_e32 v128, 0
	v_mov_b32_e32 v129, 0
	v_mov_b32_e32 v130, 0
	v_mov_b32_e32 v131, 0
	s_mov_b64 s[70:71], exec
	s_mov_b64 exec, s[76:77]
	global_load_dwordx4 v[128:131], v2, s[64:65] offset:-512 sc1 nt
	s_mov_b64 exec, s[70:71]
	v_mov_b32_e32 v132, 0
	v_mov_b32_e32 v133, 0
	v_mov_b32_e32 v134, 0
	v_mov_b32_e32 v135, 0
	s_mov_b64 s[70:71], exec
	s_mov_b64 exec, s[76:77]
	global_load_dwordx4 v[132:135], v2, s[66:67] offset:-512 sc1 nt
	s_mov_b64 exec, s[70:71]
	global_load_dwordx4 v[8:11], v2, s[52:53] sc1 nt
	global_load_dwordx4 v[12:15], v2, s[54:55] sc1 nt
	global_load_dwordx4 v[16:19], v2, s[56:57] sc1 nt
	global_load_dwordx4 v[20:23], v2, s[58:59] sc1 nt
	global_load_dwordx4 v[24:27], v2, s[60:61] sc1 nt
	global_load_dwordx4 v[28:31], v2, s[62:63] sc1 nt
	global_load_dwordx4 v[32:35], v2, s[64:65] sc1 nt
	global_load_dwordx4 v[36:39], v2, s[66:67] sc1 nt
	global_load_dwordx4 v[40:43], v2, s[52:53] offset:512 sc1 nt
	global_load_dwordx4 v[44:47], v2, s[54:55] offset:512 sc1 nt
	global_load_dwordx4 v[48:51], v2, s[56:57] offset:512 sc1 nt
	global_load_dwordx4 v[52:55], v2, s[58:59] offset:512 sc1 nt
	global_load_dwordx4 v[56:59], v2, s[60:61] offset:512 sc1 nt
	global_load_dwordx4 v[60:63], v2, s[62:63] offset:512 sc1 nt
	global_load_dwordx4 v[64:67], v2, s[64:65] offset:512 sc1 nt
	global_load_dwordx4 v[68:71], v2, s[66:67] offset:512 sc1 nt
	global_load_dwordx4 v[72:75], v2, s[52:53] offset:1024 sc1 nt
	global_load_dwordx4 v[76:79], v2, s[54:55] offset:1024 sc1 nt
	global_load_dwordx4 v[80:83], v2, s[56:57] offset:1024 sc1 nt
	global_load_dwordx4 v[84:87], v2, s[58:59] offset:1024 sc1 nt
	global_load_dwordx4 v[88:91], v2, s[60:61] offset:1024 sc1 nt
	global_load_dwordx4 v[92:95], v2, s[62:63] offset:1024 sc1 nt
	global_load_dwordx4 v[96:99], v2, s[64:65] offset:1024 sc1 nt
	global_load_dwordx4 v[100:103], v2, s[66:67] offset:1024 sc1 nt
	s_waitcnt vmcnt(31)
	v_cvt_pk_f16_f32 v4, v104, v105
	v_cvt_pk_f16_f32 v5, v106, v107
	s_mov_b64 s[70:71], exec
	s_mov_b64 exec, s[76:77]
	ds_write_b64 v144, v[4:5]
	s_mov_b64 exec, s[70:71]
	global_load_dwordx4 v[104:107], v2, s[52:53] offset:1536 sc1 nt
	s_waitcnt vmcnt(31)
	v_cvt_pk_f16_f32 v4, v108, v109
	v_cvt_pk_f16_f32 v5, v110, v111
	s_mov_b64 s[70:71], exec
	s_mov_b64 exec, s[76:77]
	ds_write_b64 v144, v[4:5] offset:2176
	s_mov_b64 exec, s[70:71]
	global_load_dwordx4 v[108:111], v2, s[54:55] offset:1536 sc1 nt
	s_waitcnt vmcnt(31)
	v_cvt_pk_f16_f32 v4, v112, v113
	v_cvt_pk_f16_f32 v5, v114, v115
	s_mov_b64 s[70:71], exec
	s_mov_b64 exec, s[76:77]
	ds_write_b64 v144, v[4:5] offset:4352
	s_mov_b64 exec, s[70:71]
	global_load_dwordx4 v[112:115], v2, s[56:57] offset:1536 sc1 nt
	s_waitcnt vmcnt(31)
	v_cvt_pk_f16_f32 v4, v116, v117
	v_cvt_pk_f16_f32 v5, v118, v119
	s_mov_b64 s[70:71], exec
	s_mov_b64 exec, s[76:77]
	ds_write_b64 v144, v[4:5] offset:6528
	s_mov_b64 exec, s[70:71]
	global_load_dwordx4 v[116:119], v2, s[58:59] offset:1536 sc1 nt
	s_waitcnt vmcnt(31)
	v_cvt_pk_f16_f32 v4, v120, v121
	v_cvt_pk_f16_f32 v5, v122, v123
	s_mov_b64 s[70:71], exec
	s_mov_b64 exec, s[76:77]
	ds_write_b64 v144, v[4:5] offset:8704
	s_mov_b64 exec, s[70:71]
	global_load_dwordx4 v[120:123], v2, s[60:61] offset:1536 sc1 nt
	s_waitcnt vmcnt(31)
	v_cvt_pk_f16_f32 v4, v124, v125
	v_cvt_pk_f16_f32 v5, v126, v127
	s_mov_b64 s[70:71], exec
	s_mov_b64 exec, s[76:77]
	ds_write_b64 v144, v[4:5] offset:10880
	s_mov_b64 exec, s[70:71]
	global_load_dwordx4 v[124:127], v2, s[62:63] offset:1536 sc1 nt
	s_waitcnt vmcnt(31)
	v_cvt_pk_f16_f32 v4, v128, v129
	v_cvt_pk_f16_f32 v5, v130, v131
	s_mov_b64 s[70:71], exec
	s_mov_b64 exec, s[76:77]
	ds_write_b64 v144, v[4:5] offset:13056
	s_mov_b64 exec, s[70:71]
	global_load_dwordx4 v[128:131], v2, s[64:65] offset:1536 sc1 nt
	s_waitcnt vmcnt(31)
	v_cvt_pk_f16_f32 v4, v132, v133
	v_cvt_pk_f16_f32 v5, v134, v135
	s_mov_b64 s[70:71], exec
	s_mov_b64 exec, s[76:77]
	ds_write_b64 v144, v[4:5] offset:15232
	s_mov_b64 exec, s[70:71]
	global_load_dwordx4 v[132:135], v2, s[66:67] offset:1536 sc1 nt
	s_waitcnt vmcnt(40)
	v_mov_b32_e32 v151, 1
	v_lshlrev_b32_e32 v160, 2, v152
	v_lshlrev_b32_e32 v161, 2, v153
	v_lshlrev_b32_e32 v162, 2, v154
	v_lshlrev_b32_e32 v163, 2, v155
	global_atomic_add v164, v160, v151, s[20:21] sc0
	global_atomic_add v165, v161, v151, s[20:21] sc0
	global_atomic_add v166, v162, v151, s[20:21] sc0
	global_atomic_add v167, v163, v151, s[20:21] sc0
	s_waitcnt vmcnt(35)
	v_cvt_pk_f16_f32 v4, v8, v9
	v_cvt_pk_f16_f32 v5, v10, v11
	ds_write_b64 v141, v[4:5]
	s_waitcnt vmcnt(27)
	v_cvt_pk_f16_f32 v4, v40, v41
	v_cvt_pk_f16_f32 v5, v42, v43
	ds_write_b64 v142, v[4:5]
	global_load_dwordx4 v[8:11], v2, s[52:53] offset:2048 sc1 nt
	global_load_dwordx4 v[40:43], v2, s[52:53] offset:2560 sc1 nt
	s_waitcnt vmcnt(36)
	v_cvt_pk_f16_f32 v4, v12, v13
	v_cvt_pk_f16_f32 v5, v14, v15
	ds_write_b64 v141, v[4:5] offset:2176
	s_waitcnt vmcnt(28)
	v_cvt_pk_f16_f32 v4, v44, v45
	v_cvt_pk_f16_f32 v5, v46, v47
	ds_write_b64 v142, v[4:5] offset:2176
	global_load_dwordx4 v[12:15], v2, s[54:55] offset:2048 sc1 nt
	global_load_dwordx4 v[44:47], v2, s[54:55] offset:2560 sc1 nt
	s_waitcnt vmcnt(37)
	v_cvt_pk_f16_f32 v4, v16, v17
	v_cvt_pk_f16_f32 v5, v18, v19
	ds_write_b64 v141, v[4:5] offset:4352
	s_waitcnt vmcnt(29)
	v_cvt_pk_f16_f32 v4, v48, v49
	v_cvt_pk_f16_f32 v5, v50, v51
	ds_write_b64 v142, v[4:5] offset:4352
	global_load_dwordx4 v[16:19], v2, s[56:57] offset:2048 sc1 nt
	global_load_dwordx4 v[48:51], v2, s[56:57] offset:2560 sc1 nt
	s_waitcnt vmcnt(38)
	v_cvt_pk_f16_f32 v4, v20, v21
	v_cvt_pk_f16_f32 v5, v22, v23
	ds_write_b64 v141, v[4:5] offset:6528
	s_waitcnt vmcnt(30)
	v_cvt_pk_f16_f32 v4, v52, v53
	v_cvt_pk_f16_f32 v5, v54, v55
	ds_write_b64 v142, v[4:5] offset:6528
	global_load_dwordx4 v[20:23], v2, s[58:59] offset:2048 sc1 nt
	global_load_dwordx4 v[52:55], v2, s[58:59] offset:2560 sc1 nt
	s_waitcnt vmcnt(39)
	v_cvt_pk_f16_f32 v4, v24, v25
	v_cvt_pk_f16_f32 v5, v26, v27
	ds_write_b64 v141, v[4:5] offset:8704
	s_waitcnt vmcnt(31)
	v_cvt_pk_f16_f32 v4, v56, v57
	v_cvt_pk_f16_f32 v5, v58, v59
	ds_write_b64 v142, v[4:5] offset:8704
	global_load_dwordx4 v[24:27], v2, s[60:61] offset:2048 sc1 nt
	global_load_dwordx4 v[56:59], v2, s[60:61] offset:2560 sc1 nt
	s_waitcnt vmcnt(40)
	v_cvt_pk_f16_f32 v4, v28, v29
	v_cvt_pk_f16_f32 v5, v30, v31
	ds_write_b64 v141, v[4:5] offset:10880
	s_waitcnt vmcnt(32)
	v_cvt_pk_f16_f32 v4, v60, v61
	v_cvt_pk_f16_f32 v5, v62, v63
	ds_write_b64 v142, v[4:5] offset:10880
	global_load_dwordx4 v[28:31], v2, s[62:63] offset:2048 sc1 nt
	global_load_dwordx4 v[60:63], v2, s[62:63] offset:2560 sc1 nt
	s_waitcnt vmcnt(41)
	v_cvt_pk_f16_f32 v4, v32, v33
	v_cvt_pk_f16_f32 v5, v34, v35
	ds_write_b64 v141, v[4:5] offset:13056
	s_waitcnt vmcnt(33)
	v_cvt_pk_f16_f32 v4, v64, v65
	v_cvt_pk_f16_f32 v5, v66, v67
	ds_write_b64 v142, v[4:5] offset:13056
	global_load_dwordx4 v[32:35], v2, s[64:65] offset:2048 sc1 nt
	global_load_dwordx4 v[64:67], v2, s[64:65] offset:2560 sc1 nt
	s_waitcnt vmcnt(42)
	v_cvt_pk_f16_f32 v4, v36, v37
	v_cvt_pk_f16_f32 v5, v38, v39
	ds_write_b64 v141, v[4:5] offset:15232
	s_waitcnt vmcnt(34)
	v_cvt_pk_f16_f32 v4, v68, v69
	v_cvt_pk_f16_f32 v5, v70, v71
	ds_write_b64 v142, v[4:5] offset:15232
	global_load_dwordx4 v[36:39], v2, s[66:67] offset:2048 sc1 nt
	global_load_dwordx4 v[68:71], v2, s[66:67] offset:2560 sc1 nt
	s_waitcnt vmcnt(0)
	v_cmp_gt_i32_e32 vcc, 64, v164
	v_lshl_add_u32 v148, v152, 6, v164
	v_lshlrev_b32_e32 v148, 2, v148
	s_and_saveexec_b64 s[2:3], vcc
	global_store_dword v148, v156, s[22:23]
	s_xor_b64 exec, exec, s[2:3]
	s_cbranch_execz .Lg1_ld_ok_0
	v_mov_b32_e32 v149, 0x8000
	global_atomic_add v149, v149, v151, s[20:21] sc0
	s_waitcnt vmcnt(0)
	v_lshlrev_b32_e32 v149, 3, v149
	v_mov_b32_e32 v160, v152
	v_mov_b32_e32 v161, v156
	global_store_dwordx2 v149, v[160:161], s[28:29]

.Lg1_ld_ok_3:
	s_mov_b64 exec, -1
	s_waitcnt lgkmcnt(0)
	s_barrier
	s_waitcnt lgkmcnt(0)
	s_barrier
	s_waitcnt vmcnt(35)
	v_cvt_pk_f16_f32 v4, v72, v73
	v_cvt_pk_f16_f32 v5, v74, v75
	ds_write_b64 v143, v[4:5]
	s_waitcnt vmcnt(27)
	v_cvt_pk_f16_f32 v4, v104, v105
	v_cvt_pk_f16_f32 v5, v106, v107
	ds_write_b64 v144, v[4:5]
	global_load_dwordx4 v[72:75], v2, s[52:53] offset:3072 sc1 nt
	global_load_dwordx4 v[104:107], v2, s[52:53] offset:3584 sc1 nt
	s_waitcnt vmcnt(36)
	v_cvt_pk_f16_f32 v4, v76, v77
	v_cvt_pk_f16_f32 v5, v78, v79
	ds_write_b64 v143, v[4:5] offset:2176
	s_waitcnt vmcnt(28)
	v_cvt_pk_f16_f32 v4, v108, v109
	v_cvt_pk_f16_f32 v5, v110, v111
	ds_write_b64 v144, v[4:5] offset:2176
	global_load_dwordx4 v[76:79], v2, s[54:55] offset:3072 sc1 nt
	global_load_dwordx4 v[108:111], v2, s[54:55] offset:3584 sc1 nt
	s_waitcnt vmcnt(37)
	v_cvt_pk_f16_f32 v4, v80, v81
	v_cvt_pk_f16_f32 v5, v82, v83
	ds_write_b64 v143, v[4:5] offset:4352
	s_waitcnt vmcnt(29)
	v_cvt_pk_f16_f32 v4, v112, v113
	v_cvt_pk_f16_f32 v5, v114, v115
	ds_write_b64 v144, v[4:5] offset:4352
	global_load_dwordx4 v[80:83], v2, s[56:57] offset:3072 sc1 nt
	global_load_dwordx4 v[112:115], v2, s[56:57] offset:3584 sc1 nt
	s_waitcnt vmcnt(38)
	v_cvt_pk_f16_f32 v4, v84, v85
	v_cvt_pk_f16_f32 v5, v86, v87
	ds_write_b64 v143, v[4:5] offset:6528
	s_waitcnt vmcnt(30)
	v_cvt_pk_f16_f32 v4, v116, v117
	v_cvt_pk_f16_f32 v5, v118, v119
	ds_write_b64 v144, v[4:5] offset:6528
	global_load_dwordx4 v[84:87], v2, s[58:59] offset:3072 sc1 nt
	global_load_dwordx4 v[116:119], v2, s[58:59] offset:3584 sc1 nt
	s_waitcnt vmcnt(39)
	v_cvt_pk_f16_f32 v4, v88, v89
	v_cvt_pk_f16_f32 v5, v90, v91
	ds_write_b64 v143, v[4:5] offset:8704
	s_waitcnt vmcnt(31)
	v_cvt_pk_f16_f32 v4, v120, v121
	v_cvt_pk_f16_f32 v5, v122, v123
	ds_write_b64 v144, v[4:5] offset:8704
	global_load_dwordx4 v[88:91], v2, s[60:61] offset:3072 sc1 nt
	global_load_dwordx4 v[120:123], v2, s[60:61] offset:3584 sc1 nt
	s_waitcnt vmcnt(40)
	v_cvt_pk_f16_f32 v4, v92, v93
	v_cvt_pk_f16_f32 v5, v94, v95
	ds_write_b64 v143, v[4:5] offset:10880
	s_waitcnt vmcnt(32)
	v_cvt_pk_f16_f32 v4, v124, v125
	v_cvt_pk_f16_f32 v5, v126, v127
	ds_write_b64 v144, v[4:5] offset:10880
	global_load_dwordx4 v[92:95], v2, s[62:63] offset:3072 sc1 nt
	global_load_dwordx4 v[124:127], v2, s[62:63] offset:3584 sc1 nt
	s_waitcnt vmcnt(41)
	v_cvt_pk_f16_f32 v4, v96, v97
	v_cvt_pk_f16_f32 v5, v98, v99
	ds_write_b64 v143, v[4:5] offset:13056
	s_waitcnt vmcnt(33)
	v_cvt_pk_f16_f32 v4, v128, v129
	v_cvt_pk_f16_f32 v5, v130, v131
	ds_write_b64 v144, v[4:5] offset:13056
	global_load_dwordx4 v[96:99], v2, s[64:65] offset:3072 sc1 nt
	global_load_dwordx4 v[128:131], v2, s[64:65] offset:3584 sc1 nt
	s_waitcnt vmcnt(42)
	v_cvt_pk_f16_f32 v4, v100, v101
	v_cvt_pk_f16_f32 v5, v102, v103
	ds_write_b64 v143, v[4:5] offset:15232
	s_waitcnt vmcnt(34)
	v_cvt_pk_f16_f32 v4, v132, v133
	v_cvt_pk_f16_f32 v5, v134, v135
	ds_write_b64 v144, v[4:5] offset:15232
	global_load_dwordx4 v[100:103], v2, s[66:67] offset:3072 sc1 nt
	global_load_dwordx4 v[132:135], v2, s[66:67] offset:3584 sc1 nt
	s_waitcnt lgkmcnt(0)
	s_barrier
	s_waitcnt lgkmcnt(0)
	s_barrier
	s_waitcnt vmcnt(31)
	v_cvt_pk_f16_f32 v4, v8, v9
	v_cvt_pk_f16_f32 v5, v10, v11
	ds_write_b64 v141, v[4:5]
	s_waitcnt vmcnt(30)
	v_cvt_pk_f16_f32 v4, v40, v41
	v_cvt_pk_f16_f32 v5, v42, v43
	ds_write_b64 v142, v[4:5]
	v_add_u32_e32 v2, 0x1000, v2
	global_load_dwordx4 v[8:11], v2, s[52:53] sc1 nt
	global_load_dwordx4 v[40:43], v2, s[52:53] offset:512 sc1 nt
	s_waitcnt vmcnt(31)
	v_cvt_pk_f16_f32 v4, v12, v13
	v_cvt_pk_f16_f32 v5, v14, v15
	ds_write_b64 v141, v[4:5] offset:2176
	s_waitcnt vmcnt(30)
	v_cvt_pk_f16_f32 v4, v44, v45
	v_cvt_pk_f16_f32 v5, v46, v47
	ds_write_b64 v142, v[4:5] offset:2176
	global_load_dwordx4 v[12:15], v2, s[54:55] sc1 nt
	global_load_dwordx4 v[44:47], v2, s[54:55] offset:512 sc1 nt
	s_waitcnt vmcnt(31)
	v_cvt_pk_f16_f32 v4, v16, v17
	v_cvt_pk_f16_f32 v5, v18, v19
	ds_write_b64 v141, v[4:5] offset:4352
	s_waitcnt vmcnt(30)
	v_cvt_pk_f16_f32 v4, v48, v49
	v_cvt_pk_f16_f32 v5, v50, v51
	ds_write_b64 v142, v[4:5] offset:4352
	global_load_dwordx4 v[16:19], v2, s[56:57] sc1 nt
	global_load_dwordx4 v[48:51], v2, s[56:57] offset:512 sc1 nt
	s_waitcnt vmcnt(31)
	v_cvt_pk_f16_f32 v4, v20, v21
	v_cvt_pk_f16_f32 v5, v22, v23
	ds_write_b64 v141, v[4:5] offset:6528
	s_waitcnt vmcnt(30)
	v_cvt_pk_f16_f32 v4, v52, v53
	v_cvt_pk_f16_f32 v5, v54, v55
	ds_write_b64 v142, v[4:5] offset:6528
	global_load_dwordx4 v[20:23], v2, s[58:59] sc1 nt
	global_load_dwordx4 v[52:55], v2, s[58:59] offset:512 sc1 nt
	s_waitcnt vmcnt(31)
	v_cvt_pk_f16_f32 v4, v24, v25
	v_cvt_pk_f16_f32 v5, v26, v27
	ds_write_b64 v141, v[4:5] offset:8704
	s_waitcnt vmcnt(30)
	v_cvt_pk_f16_f32 v4, v56, v57
	v_cvt_pk_f16_f32 v5, v58, v59
	ds_write_b64 v142, v[4:5] offset:8704
	global_load_dwordx4 v[24:27], v2, s[60:61] sc1 nt
	global_load_dwordx4 v[56:59], v2, s[60:61] offset:512 sc1 nt
	s_waitcnt vmcnt(31)
	v_cvt_pk_f16_f32 v4, v28, v29
	v_cvt_pk_f16_f32 v5, v30, v31
	ds_write_b64 v141, v[4:5] offset:10880
	s_waitcnt vmcnt(30)
	v_cvt_pk_f16_f32 v4, v60, v61
	v_cvt_pk_f16_f32 v5, v62, v63
	ds_write_b64 v142, v[4:5] offset:10880
	global_load_dwordx4 v[28:31], v2, s[62:63] sc1 nt
	global_load_dwordx4 v[60:63], v2, s[62:63] offset:512 sc1 nt
	s_waitcnt vmcnt(31)
	v_cvt_pk_f16_f32 v4, v32, v33
	v_cvt_pk_f16_f32 v5, v34, v35
	ds_write_b64 v141, v[4:5] offset:13056
	s_waitcnt vmcnt(30)
	v_cvt_pk_f16_f32 v4, v64, v65
	v_cvt_pk_f16_f32 v5, v66, v67
	ds_write_b64 v142, v[4:5] offset:13056
	global_load_dwordx4 v[32:35], v2, s[64:65] sc1 nt
	global_load_dwordx4 v[64:67], v2, s[64:65] offset:512 sc1 nt
	s_waitcnt vmcnt(31)
	v_cvt_pk_f16_f32 v4, v36, v37
	v_cvt_pk_f16_f32 v5, v38, v39
	ds_write_b64 v141, v[4:5] offset:15232
	s_waitcnt vmcnt(30)
	v_cvt_pk_f16_f32 v4, v68, v69
	v_cvt_pk_f16_f32 v5, v70, v71
	ds_write_b64 v142, v[4:5] offset:15232
	global_load_dwordx4 v[36:39], v2, s[66:67] sc1 nt
	global_load_dwordx4 v[68:71], v2, s[66:67] offset:512 sc1 nt
	s_waitcnt lgkmcnt(0)
	s_barrier
	s_waitcnt lgkmcnt(0)
	s_barrier
	s_waitcnt vmcnt(31)
	v_cvt_pk_f16_f32 v4, v72, v73
	v_cvt_pk_f16_f32 v5, v74, v75
	ds_write_b64 v143, v[4:5]
	s_waitcnt vmcnt(30)
	v_cvt_pk_f16_f32 v4, v104, v105
	v_cvt_pk_f16_f32 v5, v106, v107
	ds_write_b64 v144, v[4:5]
	global_load_dwordx4 v[72:75], v2, s[52:53] offset:1024 sc1 nt
	global_load_dwordx4 v[104:107], v2, s[52:53] offset:1536 sc1 nt
	s_waitcnt vmcnt(31)
	v_cvt_pk_f16_f32 v4, v76, v77
	v_cvt_pk_f16_f32 v5, v78, v79
	ds_write_b64 v143, v[4:5] offset:2176
	s_waitcnt vmcnt(30)
	v_cvt_pk_f16_f32 v4, v108, v109
	v_cvt_pk_f16_f32 v5, v110, v111
	ds_write_b64 v144, v[4:5] offset:2176
	global_load_dwordx4 v[76:79], v2, s[54:55] offset:1024 sc1 nt
	global_load_dwordx4 v[108:111], v2, s[54:55] offset:1536 sc1 nt
	s_waitcnt vmcnt(31)
	v_cvt_pk_f16_f32 v4, v80, v81
	v_cvt_pk_f16_f32 v5, v82, v83
	ds_write_b64 v143, v[4:5] offset:4352
	s_waitcnt vmcnt(30)
	v_cvt_pk_f16_f32 v4, v112, v113
	v_cvt_pk_f16_f32 v5, v114, v115
	ds_write_b64 v144, v[4:5] offset:4352
	global_load_dwordx4 v[80:83], v2, s[56:57] offset:1024 sc1 nt
	global_load_dwordx4 v[112:115], v2, s[56:57] offset:1536 sc1 nt
	s_waitcnt vmcnt(31)
	v_cvt_pk_f16_f32 v4, v84, v85
	v_cvt_pk_f16_f32 v5, v86, v87
	ds_write_b64 v143, v[4:5] offset:6528
	s_waitcnt vmcnt(30)
	v_cvt_pk_f16_f32 v4, v116, v117
	v_cvt_pk_f16_f32 v5, v118, v119
	ds_write_b64 v144, v[4:5] offset:6528
	global_load_dwordx4 v[84:87], v2, s[58:59] offset:1024 sc1 nt
	global_load_dwordx4 v[116:119], v2, s[58:59] offset:1536 sc1 nt
	s_waitcnt vmcnt(31)
	v_cvt_pk_f16_f32 v4, v88, v89
	v_cvt_pk_f16_f32 v5, v90, v91
	ds_write_b64 v143, v[4:5] offset:8704
	s_waitcnt vmcnt(30)
	v_cvt_pk_f16_f32 v4, v120, v121
	v_cvt_pk_f16_f32 v5, v122, v123
	ds_write_b64 v144, v[4:5] offset:8704
	global_load_dwordx4 v[88:91], v2, s[60:61] offset:1024 sc1 nt
	global_load_dwordx4 v[120:123], v2, s[60:61] offset:1536 sc1 nt
	s_waitcnt vmcnt(31)
	v_cvt_pk_f16_f32 v4, v92, v93
	v_cvt_pk_f16_f32 v5, v94, v95
	ds_write_b64 v143, v[4:5] offset:10880
	s_waitcnt vmcnt(30)
	v_cvt_pk_f16_f32 v4, v124, v125
	v_cvt_pk_f16_f32 v5, v126, v127
	ds_write_b64 v144, v[4:5] offset:10880
	global_load_dwordx4 v[92:95], v2, s[62:63] offset:1024 sc1 nt
	global_load_dwordx4 v[124:127], v2, s[62:63] offset:1536 sc1 nt
	s_waitcnt vmcnt(31)
	v_cvt_pk_f16_f32 v4, v96, v97
	v_cvt_pk_f16_f32 v5, v98, v99
	ds_write_b64 v143, v[4:5] offset:13056
	s_waitcnt vmcnt(30)
	v_cvt_pk_f16_f32 v4, v128, v129
	v_cvt_pk_f16_f32 v5, v130, v131
	ds_write_b64 v144, v[4:5] offset:13056
	global_load_dwordx4 v[96:99], v2, s[64:65] offset:1024 sc1 nt
	global_load_dwordx4 v[128:131], v2, s[64:65] offset:1536 sc1 nt
	s_waitcnt vmcnt(31)
	v_cvt_pk_f16_f32 v4, v100, v101
	v_cvt_pk_f16_f32 v5, v102, v103
	ds_write_b64 v143, v[4:5] offset:15232
	s_waitcnt vmcnt(30)
	v_cvt_pk_f16_f32 v4, v132, v133
	v_cvt_pk_f16_f32 v5, v134, v135
	ds_write_b64 v144, v[4:5] offset:15232
	global_load_dwordx4 v[100:103], v2, s[66:67] offset:1024 sc1 nt
	global_load_dwordx4 v[132:135], v2, s[66:67] offset:1536 sc1 nt
	s_waitcnt lgkmcnt(0)
	s_barrier
	s_waitcnt lgkmcnt(0)
	s_barrier
	s_waitcnt vmcnt(31)
	v_cvt_pk_f16_f32 v4, v8, v9
	v_cvt_pk_f16_f32 v5, v10, v11
	ds_write_b64 v141, v[4:5]
	s_waitcnt vmcnt(30)
	v_cvt_pk_f16_f32 v4, v40, v41
	v_cvt_pk_f16_f32 v5, v42, v43
	ds_write_b64 v142, v[4:5]
	global_load_dwordx4 v[8:11], v2, s[52:53] offset:2048 sc1 nt
	global_load_dwordx4 v[40:43], v2, s[52:53] offset:2560 sc1 nt
	s_waitcnt vmcnt(31)
	v_cvt_pk_f16_f32 v4, v12, v13
	v_cvt_pk_f16_f32 v5, v14, v15
	ds_write_b64 v141, v[4:5] offset:2176
	s_waitcnt vmcnt(30)
	v_cvt_pk_f16_f32 v4, v44, v45
	v_cvt_pk_f16_f32 v5, v46, v47
	ds_write_b64 v142, v[4:5] offset:2176
	global_load_dwordx4 v[12:15], v2, s[54:55] offset:2048 sc1 nt
	global_load_dwordx4 v[44:47], v2, s[54:55] offset:2560 sc1 nt
	s_waitcnt vmcnt(31)
	v_cvt_pk_f16_f32 v4, v16, v17
	v_cvt_pk_f16_f32 v5, v18, v19
	ds_write_b64 v141, v[4:5] offset:4352
	s_waitcnt vmcnt(30)
	v_cvt_pk_f16_f32 v4, v48, v49
	v_cvt_pk_f16_f32 v5, v50, v51
	ds_write_b64 v142, v[4:5] offset:4352
	global_load_dwordx4 v[16:19], v2, s[56:57] offset:2048 sc1 nt
	global_load_dwordx4 v[48:51], v2, s[56:57] offset:2560 sc1 nt
	s_waitcnt vmcnt(31)
	v_cvt_pk_f16_f32 v4, v20, v21
	v_cvt_pk_f16_f32 v5, v22, v23
	ds_write_b64 v141, v[4:5] offset:6528
	s_waitcnt vmcnt(30)
	v_cvt_pk_f16_f32 v4, v52, v53
	v_cvt_pk_f16_f32 v5, v54, v55
	ds_write_b64 v142, v[4:5] offset:6528
	global_load_dwordx4 v[20:23], v2, s[58:59] offset:2048 sc1 nt
	global_load_dwordx4 v[52:55], v2, s[58:59] offset:2560 sc1 nt
	s_waitcnt vmcnt(31)
	v_cvt_pk_f16_f32 v4, v24, v25
	v_cvt_pk_f16_f32 v5, v26, v27
	ds_write_b64 v141, v[4:5] offset:8704
	s_waitcnt vmcnt(30)
	v_cvt_pk_f16_f32 v4, v56, v57
	v_cvt_pk_f16_f32 v5, v58, v59
	ds_write_b64 v142, v[4:5] offset:8704
	global_load_dwordx4 v[24:27], v2, s[60:61] offset:2048 sc1 nt
	global_load_dwordx4 v[56:59], v2, s[60:61] offset:2560 sc1 nt
	s_waitcnt vmcnt(31)
	v_cvt_pk_f16_f32 v4, v28, v29
	v_cvt_pk_f16_f32 v5, v30, v31
	ds_write_b64 v141, v[4:5] offset:10880
	s_waitcnt vmcnt(30)
	v_cvt_pk_f16_f32 v4, v60, v61
	v_cvt_pk_f16_f32 v5, v62, v63
	ds_write_b64 v142, v[4:5] offset:10880
	global_load_dwordx4 v[28:31], v2, s[62:63] offset:2048 sc1 nt
	global_load_dwordx4 v[60:63], v2, s[62:63] offset:2560 sc1 nt
	s_waitcnt vmcnt(31)
	v_cvt_pk_f16_f32 v4, v32, v33
	v_cvt_pk_f16_f32 v5, v34, v35
	ds_write_b64 v141, v[4:5] offset:13056
	s_waitcnt vmcnt(30)
	v_cvt_pk_f16_f32 v4, v64, v65
	v_cvt_pk_f16_f32 v5, v66, v67
	ds_write_b64 v142, v[4:5] offset:13056
	global_load_dwordx4 v[32:35], v2, s[64:65] offset:2048 sc1 nt
	global_load_dwordx4 v[64:67], v2, s[64:65] offset:2560 sc1 nt
	s_waitcnt vmcnt(31)
	v_cvt_pk_f16_f32 v4, v36, v37
	v_cvt_pk_f16_f32 v5, v38, v39
	ds_write_b64 v141, v[4:5] offset:15232
	s_waitcnt vmcnt(30)
	v_cvt_pk_f16_f32 v4, v68, v69
	v_cvt_pk_f16_f32 v5, v70, v71
	ds_write_b64 v142, v[4:5] offset:15232
	global_load_dwordx4 v[36:39], v2, s[66:67] offset:2048 sc1 nt
	global_load_dwordx4 v[68:71], v2, s[66:67] offset:2560 sc1 nt
	s_waitcnt lgkmcnt(0)
	s_barrier
	s_waitcnt lgkmcnt(0)
	s_barrier
	s_waitcnt vmcnt(31)
	v_cvt_pk_f16_f32 v4, v72, v73
	v_cvt_pk_f16_f32 v5, v74, v75
	ds_write_b64 v143, v[4:5]
	s_waitcnt vmcnt(30)
	v_cvt_pk_f16_f32 v4, v104, v105
	v_cvt_pk_f16_f32 v5, v106, v107
	ds_write_b64 v144, v[4:5]
	global_load_dwordx4 v[72:75], v2, s[52:53] offset:3072 sc1 nt
	global_load_dwordx4 v[104:107], v2, s[52:53] offset:3584 sc1 nt
	s_waitcnt vmcnt(31)
	v_cvt_pk_f16_f32 v4, v76, v77
	v_cvt_pk_f16_f32 v5, v78, v79
	ds_write_b64 v143, v[4:5] offset:2176
	s_waitcnt vmcnt(30)
	v_cvt_pk_f16_f32 v4, v108, v109
	v_cvt_pk_f16_f32 v5, v110, v111
	ds_write_b64 v144, v[4:5] offset:2176
	global_load_dwordx4 v[76:79], v2, s[54:55] offset:3072 sc1 nt
	global_load_dwordx4 v[108:111], v2, s[54:55] offset:3584 sc1 nt
	s_waitcnt vmcnt(31)
	v_cvt_pk_f16_f32 v4, v80, v81
	v_cvt_pk_f16_f32 v5, v82, v83
	ds_write_b64 v143, v[4:5] offset:4352
	s_waitcnt vmcnt(30)
	v_cvt_pk_f16_f32 v4, v112, v113
	v_cvt_pk_f16_f32 v5, v114, v115
	ds_write_b64 v144, v[4:5] offset:4352
	global_load_dwordx4 v[80:83], v2, s[56:57] offset:3072 sc1 nt
	global_load_dwordx4 v[112:115], v2, s[56:57] offset:3584 sc1 nt
	s_waitcnt vmcnt(31)
	v_cvt_pk_f16_f32 v4, v84, v85
	v_cvt_pk_f16_f32 v5, v86, v87
	ds_write_b64 v143, v[4:5] offset:6528
	s_waitcnt vmcnt(30)
	v_cvt_pk_f16_f32 v4, v116, v117
	v_cvt_pk_f16_f32 v5, v118, v119
	ds_write_b64 v144, v[4:5] offset:6528
	global_load_dwordx4 v[84:87], v2, s[58:59] offset:3072 sc1 nt
	global_load_dwordx4 v[116:119], v2, s[58:59] offset:3584 sc1 nt
	s_waitcnt vmcnt(31)
	v_cvt_pk_f16_f32 v4, v88, v89
	v_cvt_pk_f16_f32 v5, v90, v91
	ds_write_b64 v143, v[4:5] offset:8704
	s_waitcnt vmcnt(30)
	v_cvt_pk_f16_f32 v4, v120, v121
	v_cvt_pk_f16_f32 v5, v122, v123
	ds_write_b64 v144, v[4:5] offset:8704
	global_load_dwordx4 v[88:91], v2, s[60:61] offset:3072 sc1 nt
	global_load_dwordx4 v[120:123], v2, s[60:61] offset:3584 sc1 nt
	s_waitcnt vmcnt(31)
	v_cvt_pk_f16_f32 v4, v92, v93
	v_cvt_pk_f16_f32 v5, v94, v95
	ds_write_b64 v143, v[4:5] offset:10880
	s_waitcnt vmcnt(30)
	v_cvt_pk_f16_f32 v4, v124, v125
	v_cvt_pk_f16_f32 v5, v126, v127
	ds_write_b64 v144, v[4:5] offset:10880
	global_load_dwordx4 v[92:95], v2, s[62:63] offset:3072 sc1 nt
	global_load_dwordx4 v[124:127], v2, s[62:63] offset:3584 sc1 nt
	s_waitcnt vmcnt(31)
	v_cvt_pk_f16_f32 v4, v96, v97
	v_cvt_pk_f16_f32 v5, v98, v99
	ds_write_b64 v143, v[4:5] offset:13056
	s_waitcnt vmcnt(30)
	v_cvt_pk_f16_f32 v4, v128, v129
	v_cvt_pk_f16_f32 v5, v130, v131
	ds_write_b64 v144, v[4:5] offset:13056
	global_load_dwordx4 v[96:99], v2, s[64:65] offset:3072 sc1 nt
	global_load_dwordx4 v[128:131], v2, s[64:65] offset:3584 sc1 nt
	s_waitcnt vmcnt(31)
	v_cvt_pk_f16_f32 v4, v100, v101
	v_cvt_pk_f16_f32 v5, v102, v103
	ds_write_b64 v143, v[4:5] offset:15232
	s_waitcnt vmcnt(30)
	v_cvt_pk_f16_f32 v4, v132, v133
	v_cvt_pk_f16_f32 v5, v134, v135
	ds_write_b64 v144, v[4:5] offset:15232
	global_load_dwordx4 v[100:103], v2, s[66:67] offset:3072 sc1 nt
	global_load_dwordx4 v[132:135], v2, s[66:67] offset:3584 sc1 nt
	s_waitcnt lgkmcnt(0)
	s_barrier
	s_waitcnt lgkmcnt(0)
	s_barrier
	s_waitcnt vmcnt(31)
	v_cvt_pk_f16_f32 v4, v8, v9
	v_cvt_pk_f16_f32 v5, v10, v11
	ds_write_b64 v141, v[4:5]
	s_waitcnt vmcnt(30)
	v_cvt_pk_f16_f32 v4, v40, v41
	v_cvt_pk_f16_f32 v5, v42, v43
	ds_write_b64 v142, v[4:5]
	v_add_u32_e32 v2, 0x1000, v2
	global_load_dwordx4 v[8:11], v2, s[52:53] sc1 nt
	global_load_dwordx4 v[40:43], v2, s[52:53] offset:512 sc1 nt
	s_waitcnt vmcnt(31)
	v_cvt_pk_f16_f32 v4, v12, v13
	v_cvt_pk_f16_f32 v5, v14, v15
	ds_write_b64 v141, v[4:5] offset:2176
	s_waitcnt vmcnt(30)
	v_cvt_pk_f16_f32 v4, v44, v45
	v_cvt_pk_f16_f32 v5, v46, v47
	ds_write_b64 v142, v[4:5] offset:2176
	global_load_dwordx4 v[12:15], v2, s[54:55] sc1 nt
	global_load_dwordx4 v[44:47], v2, s[54:55] offset:512 sc1 nt
	s_waitcnt vmcnt(31)
	v_cvt_pk_f16_f32 v4, v16, v17
	v_cvt_pk_f16_f32 v5, v18, v19
	ds_write_b64 v141, v[4:5] offset:4352
	s_waitcnt vmcnt(30)
	v_cvt_pk_f16_f32 v4, v48, v49
	v_cvt_pk_f16_f32 v5, v50, v51
	ds_write_b64 v142, v[4:5] offset:4352
	global_load_dwordx4 v[16:19], v2, s[56:57] sc1 nt
	global_load_dwordx4 v[48:51], v2, s[56:57] offset:512 sc1 nt
	s_waitcnt vmcnt(31)
	v_cvt_pk_f16_f32 v4, v20, v21
	v_cvt_pk_f16_f32 v5, v22, v23
	ds_write_b64 v141, v[4:5] offset:6528
	s_waitcnt vmcnt(30)
	v_cvt_pk_f16_f32 v4, v52, v53
	v_cvt_pk_f16_f32 v5, v54, v55
	ds_write_b64 v142, v[4:5] offset:6528
	global_load_dwordx4 v[20:23], v2, s[58:59] sc1 nt
	global_load_dwordx4 v[52:55], v2, s[58:59] offset:512 sc1 nt
	s_waitcnt vmcnt(31)
	v_cvt_pk_f16_f32 v4, v24, v25
	v_cvt_pk_f16_f32 v5, v26, v27
	ds_write_b64 v141, v[4:5] offset:8704
	s_waitcnt vmcnt(30)
	v_cvt_pk_f16_f32 v4, v56, v57
	v_cvt_pk_f16_f32 v5, v58, v59
	ds_write_b64 v142, v[4:5] offset:8704
	global_load_dwordx4 v[24:27], v2, s[60:61] sc1 nt
	global_load_dwordx4 v[56:59], v2, s[60:61] offset:512 sc1 nt
	s_waitcnt vmcnt(31)
	v_cvt_pk_f16_f32 v4, v28, v29
	v_cvt_pk_f16_f32 v5, v30, v31
	ds_write_b64 v141, v[4:5] offset:10880
	s_waitcnt vmcnt(30)
	v_cvt_pk_f16_f32 v4, v60, v61
	v_cvt_pk_f16_f32 v5, v62, v63
	ds_write_b64 v142, v[4:5] offset:10880
	global_load_dwordx4 v[28:31], v2, s[62:63] sc1 nt
	global_load_dwordx4 v[60:63], v2, s[62:63] offset:512 sc1 nt
	s_waitcnt vmcnt(31)
	v_cvt_pk_f16_f32 v4, v32, v33
	v_cvt_pk_f16_f32 v5, v34, v35
	ds_write_b64 v141, v[4:5] offset:13056
	s_waitcnt vmcnt(30)
	v_cvt_pk_f16_f32 v4, v64, v65
	v_cvt_pk_f16_f32 v5, v66, v67
	ds_write_b64 v142, v[4:5] offset:13056
	global_load_dwordx4 v[32:35], v2, s[64:65] sc1 nt
	global_load_dwordx4 v[64:67], v2, s[64:65] offset:512 sc1 nt
	s_waitcnt vmcnt(31)
	v_cvt_pk_f16_f32 v4, v36, v37
	v_cvt_pk_f16_f32 v5, v38, v39
	ds_write_b64 v141, v[4:5] offset:15232
	s_waitcnt vmcnt(30)
	v_cvt_pk_f16_f32 v4, v68, v69
	v_cvt_pk_f16_f32 v5, v70, v71
	ds_write_b64 v142, v[4:5] offset:15232
	global_load_dwordx4 v[36:39], v2, s[66:67] sc1 nt
	global_load_dwordx4 v[68:71], v2, s[66:67] offset:512 sc1 nt
	s_waitcnt lgkmcnt(0)
	s_barrier
	s_waitcnt lgkmcnt(0)
	s_barrier
	s_waitcnt vmcnt(31)
	v_cvt_pk_f16_f32 v4, v72, v73
	v_cvt_pk_f16_f32 v5, v74, v75
	ds_write_b64 v143, v[4:5]
	s_waitcnt vmcnt(30)
	v_cvt_pk_f16_f32 v4, v104, v105
	v_cvt_pk_f16_f32 v5, v106, v107
	ds_write_b64 v144, v[4:5]
	global_load_dwordx4 v[72:75], v2, s[52:53] offset:1024 sc1 nt
	global_load_dwordx4 v[104:107], v2, s[52:53] offset:1536 sc1 nt
	s_waitcnt vmcnt(31)
	v_cvt_pk_f16_f32 v4, v76, v77
	v_cvt_pk_f16_f32 v5, v78, v79
	ds_write_b64 v143, v[4:5] offset:2176
	s_waitcnt vmcnt(30)
	v_cvt_pk_f16_f32 v4, v108, v109
	v_cvt_pk_f16_f32 v5, v110, v111
	ds_write_b64 v144, v[4:5] offset:2176
	global_load_dwordx4 v[76:79], v2, s[54:55] offset:1024 sc1 nt
	global_load_dwordx4 v[108:111], v2, s[54:55] offset:1536 sc1 nt
	s_waitcnt vmcnt(31)
	v_cvt_pk_f16_f32 v4, v80, v81
	v_cvt_pk_f16_f32 v5, v82, v83
	ds_write_b64 v143, v[4:5] offset:4352
	s_waitcnt vmcnt(30)
	v_cvt_pk_f16_f32 v4, v112, v113
	v_cvt_pk_f16_f32 v5, v114, v115
	ds_write_b64 v144, v[4:5] offset:4352
	global_load_dwordx4 v[80:83], v2, s[56:57] offset:1024 sc1 nt
	global_load_dwordx4 v[112:115], v2, s[56:57] offset:1536 sc1 nt
	s_waitcnt vmcnt(31)
	v_cvt_pk_f16_f32 v4, v84, v85
	v_cvt_pk_f16_f32 v5, v86, v87
	ds_write_b64 v143, v[4:5] offset:6528
	s_waitcnt vmcnt(30)
	v_cvt_pk_f16_f32 v4, v116, v117
	v_cvt_pk_f16_f32 v5, v118, v119
	ds_write_b64 v144, v[4:5] offset:6528
	global_load_dwordx4 v[84:87], v2, s[58:59] offset:1024 sc1 nt
	global_load_dwordx4 v[116:119], v2, s[58:59] offset:1536 sc1 nt
	s_waitcnt vmcnt(31)
	v_cvt_pk_f16_f32 v4, v88, v89
	v_cvt_pk_f16_f32 v5, v90, v91
	ds_write_b64 v143, v[4:5] offset:8704
	s_waitcnt vmcnt(30)
	v_cvt_pk_f16_f32 v4, v120, v121
	v_cvt_pk_f16_f32 v5, v122, v123
	ds_write_b64 v144, v[4:5] offset:8704
	global_load_dwordx4 v[88:91], v2, s[60:61] offset:1024 sc1 nt
	global_load_dwordx4 v[120:123], v2, s[60:61] offset:1536 sc1 nt
	s_waitcnt vmcnt(31)
	v_cvt_pk_f16_f32 v4, v92, v93
	v_cvt_pk_f16_f32 v5, v94, v95
	ds_write_b64 v143, v[4:5] offset:10880
	s_waitcnt vmcnt(30)
	v_cvt_pk_f16_f32 v4, v124, v125
	v_cvt_pk_f16_f32 v5, v126, v127
	ds_write_b64 v144, v[4:5] offset:10880
	global_load_dwordx4 v[92:95], v2, s[62:63] offset:1024 sc1 nt
	global_load_dwordx4 v[124:127], v2, s[62:63] offset:1536 sc1 nt
	s_waitcnt vmcnt(31)
	v_cvt_pk_f16_f32 v4, v96, v97
	v_cvt_pk_f16_f32 v5, v98, v99
	ds_write_b64 v143, v[4:5] offset:13056
	s_waitcnt vmcnt(30)
	v_cvt_pk_f16_f32 v4, v128, v129
	v_cvt_pk_f16_f32 v5, v130, v131
	ds_write_b64 v144, v[4:5] offset:13056
	global_load_dwordx4 v[96:99], v2, s[64:65] offset:1024 sc1 nt
	global_load_dwordx4 v[128:131], v2, s[64:65] offset:1536 sc1 nt
	s_waitcnt vmcnt(31)
	v_cvt_pk_f16_f32 v4, v100, v101
	v_cvt_pk_f16_f32 v5, v102, v103
	ds_write_b64 v143, v[4:5] offset:15232
	s_waitcnt vmcnt(30)
	v_cvt_pk_f16_f32 v4, v132, v133
	v_cvt_pk_f16_f32 v5, v134, v135
	ds_write_b64 v144, v[4:5] offset:15232
	global_load_dwordx4 v[100:103], v2, s[66:67] offset:1024 sc1 nt
	global_load_dwordx4 v[132:135], v2, s[66:67] offset:1536 sc1 nt
	s_waitcnt lgkmcnt(0)
	s_barrier
	s_waitcnt lgkmcnt(0)
	s_barrier
	s_waitcnt vmcnt(31)
	v_cvt_pk_f16_f32 v4, v8, v9
	v_cvt_pk_f16_f32 v5, v10, v11
	ds_write_b64 v141, v[4:5]
	s_waitcnt vmcnt(30)
	v_cvt_pk_f16_f32 v4, v40, v41
	v_cvt_pk_f16_f32 v5, v42, v43
	ds_write_b64 v142, v[4:5]
	global_load_dwordx4 v[8:11], v2, s[52:53] offset:2048 sc1 nt
	global_load_dwordx4 v[40:43], v2, s[52:53] offset:2560 sc1 nt
	s_waitcnt vmcnt(31)
	v_cvt_pk_f16_f32 v4, v12, v13
	v_cvt_pk_f16_f32 v5, v14, v15
	ds_write_b64 v141, v[4:5] offset:2176
	s_waitcnt vmcnt(30)
	v_cvt_pk_f16_f32 v4, v44, v45
	v_cvt_pk_f16_f32 v5, v46, v47
	ds_write_b64 v142, v[4:5] offset:2176
	global_load_dwordx4 v[12:15], v2, s[54:55] offset:2048 sc1 nt
	global_load_dwordx4 v[44:47], v2, s[54:55] offset:2560 sc1 nt
	s_waitcnt vmcnt(31)
	v_cvt_pk_f16_f32 v4, v16, v17
	v_cvt_pk_f16_f32 v5, v18, v19
	ds_write_b64 v141, v[4:5] offset:4352
	s_waitcnt vmcnt(30)
	v_cvt_pk_f16_f32 v4, v48, v49
	v_cvt_pk_f16_f32 v5, v50, v51
	ds_write_b64 v142, v[4:5] offset:4352
	global_load_dwordx4 v[16:19], v2, s[56:57] offset:2048 sc1 nt
	global_load_dwordx4 v[48:51], v2, s[56:57] offset:2560 sc1 nt
	s_waitcnt vmcnt(31)
	v_cvt_pk_f16_f32 v4, v20, v21
	v_cvt_pk_f16_f32 v5, v22, v23
	ds_write_b64 v141, v[4:5] offset:6528
	s_waitcnt vmcnt(30)
	v_cvt_pk_f16_f32 v4, v52, v53
	v_cvt_pk_f16_f32 v5, v54, v55
	ds_write_b64 v142, v[4:5] offset:6528
	global_load_dwordx4 v[20:23], v2, s[58:59] offset:2048 sc1 nt
	global_load_dwordx4 v[52:55], v2, s[58:59] offset:2560 sc1 nt
	s_waitcnt vmcnt(31)
	v_cvt_pk_f16_f32 v4, v24, v25
	v_cvt_pk_f16_f32 v5, v26, v27
	ds_write_b64 v141, v[4:5] offset:8704
	s_waitcnt vmcnt(30)
	v_cvt_pk_f16_f32 v4, v56, v57
	v_cvt_pk_f16_f32 v5, v58, v59
	ds_write_b64 v142, v[4:5] offset:8704
	global_load_dwordx4 v[24:27], v2, s[60:61] offset:2048 sc1 nt
	global_load_dwordx4 v[56:59], v2, s[60:61] offset:2560 sc1 nt
	s_waitcnt vmcnt(31)
	v_cvt_pk_f16_f32 v4, v28, v29
	v_cvt_pk_f16_f32 v5, v30, v31
	ds_write_b64 v141, v[4:5] offset:10880
	s_waitcnt vmcnt(30)
	v_cvt_pk_f16_f32 v4, v60, v61
	v_cvt_pk_f16_f32 v5, v62, v63
	ds_write_b64 v142, v[4:5] offset:10880
	global_load_dwordx4 v[28:31], v2, s[62:63] offset:2048 sc1 nt
	global_load_dwordx4 v[60:63], v2, s[62:63] offset:2560 sc1 nt
	s_waitcnt vmcnt(31)
	v_cvt_pk_f16_f32 v4, v32, v33
	v_cvt_pk_f16_f32 v5, v34, v35
	ds_write_b64 v141, v[4:5] offset:13056
	s_waitcnt vmcnt(30)
	v_cvt_pk_f16_f32 v4, v64, v65
	v_cvt_pk_f16_f32 v5, v66, v67
	ds_write_b64 v142, v[4:5] offset:13056
	global_load_dwordx4 v[32:35], v2, s[64:65] offset:2048 sc1 nt
	global_load_dwordx4 v[64:67], v2, s[64:65] offset:2560 sc1 nt
	s_waitcnt vmcnt(31)
	v_cvt_pk_f16_f32 v4, v36, v37
	v_cvt_pk_f16_f32 v5, v38, v39
	ds_write_b64 v141, v[4:5] offset:15232
	s_waitcnt vmcnt(30)
	v_cvt_pk_f16_f32 v4, v68, v69
	v_cvt_pk_f16_f32 v5, v70, v71
	ds_write_b64 v142, v[4:5] offset:15232
	global_load_dwordx4 v[36:39], v2, s[66:67] offset:2048 sc1 nt
	global_load_dwordx4 v[68:71], v2, s[66:67] offset:2560 sc1 nt
	s_waitcnt lgkmcnt(0)
	s_barrier
	s_waitcnt lgkmcnt(0)
	s_barrier
	s_waitcnt vmcnt(31)
	v_cvt_pk_f16_f32 v4, v72, v73
	v_cvt_pk_f16_f32 v5, v74, v75
	ds_write_b64 v143, v[4:5]
	s_waitcnt vmcnt(30)
	v_cvt_pk_f16_f32 v4, v104, v105
	v_cvt_pk_f16_f32 v5, v106, v107
	ds_write_b64 v144, v[4:5]
	global_load_dwordx4 v[72:75], v2, s[52:53] offset:3072 sc1 nt
	v_mov_b32_e32 v104, 0
	v_mov_b32_e32 v105, 0
	v_mov_b32_e32 v106, 0
	v_mov_b32_e32 v107, 0
	s_mov_b64 s[70:71], exec
	s_mov_b64 exec, s[68:69]
	global_load_dwordx4 v[104:107], v2, s[52:53] offset:3584 sc1 nt
	s_mov_b64 exec, s[70:71]
	s_waitcnt vmcnt(31)
	v_cvt_pk_f16_f32 v4, v76, v77
	v_cvt_pk_f16_f32 v5, v78, v79
	ds_write_b64 v143, v[4:5] offset:2176
	s_waitcnt vmcnt(30)
	v_cvt_pk_f16_f32 v4, v108, v109
	v_cvt_pk_f16_f32 v5, v110, v111
	ds_write_b64 v144, v[4:5] offset:2176
	global_load_dwordx4 v[76:79], v2, s[54:55] offset:3072 sc1 nt
	v_mov_b32_e32 v108, 0
	v_mov_b32_e32 v109, 0
	v_mov_b32_e32 v110, 0
	v_mov_b32_e32 v111, 0
	s_mov_b64 s[70:71], exec
	s_mov_b64 exec, s[68:69]
	global_load_dwordx4 v[108:111], v2, s[54:55] offset:3584 sc1 nt
	s_mov_b64 exec, s[70:71]
	s_waitcnt vmcnt(31)
	v_cvt_pk_f16_f32 v4, v80, v81
	v_cvt_pk_f16_f32 v5, v82, v83
	ds_write_b64 v143, v[4:5] offset:4352
	s_waitcnt vmcnt(30)
	v_cvt_pk_f16_f32 v4, v112, v113
	v_cvt_pk_f16_f32 v5, v114, v115
	ds_write_b64 v144, v[4:5] offset:4352
	global_load_dwordx4 v[80:83], v2, s[56:57] offset:3072 sc1 nt
	v_mov_b32_e32 v112, 0
	v_mov_b32_e32 v113, 0
	v_mov_b32_e32 v114, 0
	v_mov_b32_e32 v115, 0
	s_mov_b64 s[70:71], exec
	s_mov_b64 exec, s[68:69]
	global_load_dwordx4 v[112:115], v2, s[56:57] offset:3584 sc1 nt
	s_mov_b64 exec, s[70:71]
	s_waitcnt vmcnt(31)
	v_cvt_pk_f16_f32 v4, v84, v85
	v_cvt_pk_f16_f32 v5, v86, v87
	ds_write_b64 v143, v[4:5] offset:6528
	s_waitcnt vmcnt(30)
	v_cvt_pk_f16_f32 v4, v116, v117
	v_cvt_pk_f16_f32 v5, v118, v119
	ds_write_b64 v144, v[4:5] offset:6528
	global_load_dwordx4 v[84:87], v2, s[58:59] offset:3072 sc1 nt
	v_mov_b32_e32 v116, 0
	v_mov_b32_e32 v117, 0
	v_mov_b32_e32 v118, 0
	v_mov_b32_e32 v119, 0
	s_mov_b64 s[70:71], exec
	s_mov_b64 exec, s[68:69]
	global_load_dwordx4 v[116:119], v2, s[58:59] offset:3584 sc1 nt
	s_mov_b64 exec, s[70:71]
	s_waitcnt vmcnt(31)
	v_cvt_pk_f16_f32 v4, v88, v89
	v_cvt_pk_f16_f32 v5, v90, v91
	ds_write_b64 v143, v[4:5] offset:8704
	s_waitcnt vmcnt(30)
	v_cvt_pk_f16_f32 v4, v120, v121
	v_cvt_pk_f16_f32 v5, v122, v123
	ds_write_b64 v144, v[4:5] offset:8704
	global_load_dwordx4 v[88:91], v2, s[60:61] offset:3072 sc1 nt
	v_mov_b32_e32 v120, 0
	v_mov_b32_e32 v121, 0
	v_mov_b32_e32 v122, 0
	v_mov_b32_e32 v123, 0
	s_mov_b64 s[70:71], exec
	s_mov_b64 exec, s[68:69]
	global_load_dwordx4 v[120:123], v2, s[60:61] offset:3584 sc1 nt
	s_mov_b64 exec, s[70:71]
	s_waitcnt vmcnt(31)
	v_cvt_pk_f16_f32 v4, v92, v93
	v_cvt_pk_f16_f32 v5, v94, v95
	ds_write_b64 v143, v[4:5] offset:10880
	s_waitcnt vmcnt(30)
	v_cvt_pk_f16_f32 v4, v124, v125
	v_cvt_pk_f16_f32 v5, v126, v127
	ds_write_b64 v144, v[4:5] offset:10880
	global_load_dwordx4 v[92:95], v2, s[62:63] offset:3072 sc1 nt
	v_mov_b32_e32 v124, 0
	v_mov_b32_e32 v125, 0
	v_mov_b32_e32 v126, 0
	v_mov_b32_e32 v127, 0
	s_mov_b64 s[70:71], exec
	s_mov_b64 exec, s[68:69]
	global_load_dwordx4 v[124:127], v2, s[62:63] offset:3584 sc1 nt
	s_mov_b64 exec, s[70:71]
	s_waitcnt vmcnt(31)
	v_cvt_pk_f16_f32 v4, v96, v97
	v_cvt_pk_f16_f32 v5, v98, v99
	ds_write_b64 v143, v[4:5] offset:13056
	s_waitcnt vmcnt(30)
	v_cvt_pk_f16_f32 v4, v128, v129
	v_cvt_pk_f16_f32 v5, v130, v131
	ds_write_b64 v144, v[4:5] offset:13056
	global_load_dwordx4 v[96:99], v2, s[64:65] offset:3072 sc1 nt
	v_mov_b32_e32 v128, 0
	v_mov_b32_e32 v129, 0
	v_mov_b32_e32 v130, 0
	v_mov_b32_e32 v131, 0
	s_mov_b64 s[70:71], exec
	s_mov_b64 exec, s[68:69]
	global_load_dwordx4 v[128:131], v2, s[64:65] offset:3584 sc1 nt
	s_mov_b64 exec, s[70:71]
	s_waitcnt vmcnt(31)
	v_cvt_pk_f16_f32 v4, v100, v101
	v_cvt_pk_f16_f32 v5, v102, v103
	ds_write_b64 v143, v[4:5] offset:15232
	s_waitcnt vmcnt(30)
	v_cvt_pk_f16_f32 v4, v132, v133
	v_cvt_pk_f16_f32 v5, v134, v135
	ds_write_b64 v144, v[4:5] offset:15232
	global_load_dwordx4 v[100:103], v2, s[66:67] offset:3072 sc1 nt
	v_mov_b32_e32 v132, 0
	v_mov_b32_e32 v133, 0
	v_mov_b32_e32 v134, 0
	v_mov_b32_e32 v135, 0
	s_mov_b64 s[70:71], exec
	s_mov_b64 exec, s[68:69]
	global_load_dwordx4 v[132:135], v2, s[66:67] offset:3584 sc1 nt
	s_mov_b64 exec, s[70:71]
	s_waitcnt lgkmcnt(0)
	s_barrier
	s_waitcnt lgkmcnt(0)
	s_barrier
	s_waitcnt vmcnt(31)
	v_cvt_pk_f16_f32 v4, v8, v9
	v_cvt_pk_f16_f32 v5, v10, v11
	ds_write_b64 v141, v[4:5]
	s_waitcnt vmcnt(30)
	v_cvt_pk_f16_f32 v4, v40, v41
	v_cvt_pk_f16_f32 v5, v42, v43
	ds_write_b64 v142, v[4:5]
	s_waitcnt vmcnt(29)
	v_cvt_pk_f16_f32 v4, v12, v13
	v_cvt_pk_f16_f32 v5, v14, v15
	ds_write_b64 v141, v[4:5] offset:2176
	s_waitcnt vmcnt(28)
	v_cvt_pk_f16_f32 v4, v44, v45
	v_cvt_pk_f16_f32 v5, v46, v47
	ds_write_b64 v142, v[4:5] offset:2176
	s_waitcnt vmcnt(27)
	v_cvt_pk_f16_f32 v4, v16, v17
	v_cvt_pk_f16_f32 v5, v18, v19
	ds_write_b64 v141, v[4:5] offset:4352
	s_waitcnt vmcnt(26)
	v_cvt_pk_f16_f32 v4, v48, v49
	v_cvt_pk_f16_f32 v5, v50, v51
	ds_write_b64 v142, v[4:5] offset:4352
	s_waitcnt vmcnt(25)
	v_cvt_pk_f16_f32 v4, v20, v21
	v_cvt_pk_f16_f32 v5, v22, v23
	ds_write_b64 v141, v[4:5] offset:6528
	s_waitcnt vmcnt(24)
	v_cvt_pk_f16_f32 v4, v52, v53
	v_cvt_pk_f16_f32 v5, v54, v55
	ds_write_b64 v142, v[4:5] offset:6528
	s_waitcnt vmcnt(23)
	v_cvt_pk_f16_f32 v4, v24, v25
	v_cvt_pk_f16_f32 v5, v26, v27
	ds_write_b64 v141, v[4:5] offset:8704
	s_waitcnt vmcnt(22)
	v_cvt_pk_f16_f32 v4, v56, v57
	v_cvt_pk_f16_f32 v5, v58, v59
	ds_write_b64 v142, v[4:5] offset:8704
	s_waitcnt vmcnt(21)
	v_cvt_pk_f16_f32 v4, v28, v29
	v_cvt_pk_f16_f32 v5, v30, v31
	ds_write_b64 v141, v[4:5] offset:10880
	s_waitcnt vmcnt(20)
	v_cvt_pk_f16_f32 v4, v60, v61
	v_cvt_pk_f16_f32 v5, v62, v63
	ds_write_b64 v142, v[4:5] offset:10880
	s_waitcnt vmcnt(19)
	v_cvt_pk_f16_f32 v4, v32, v33
	v_cvt_pk_f16_f32 v5, v34, v35
	ds_write_b64 v141, v[4:5] offset:13056
	s_waitcnt vmcnt(18)
	v_cvt_pk_f16_f32 v4, v64, v65
	v_cvt_pk_f16_f32 v5, v66, v67
	ds_write_b64 v142, v[4:5] offset:13056
	s_waitcnt vmcnt(17)
	v_cvt_pk_f16_f32 v4, v36, v37
	v_cvt_pk_f16_f32 v5, v38, v39
	ds_write_b64 v141, v[4:5] offset:15232
	s_waitcnt vmcnt(16)
	v_cvt_pk_f16_f32 v4, v68, v69
	v_cvt_pk_f16_f32 v5, v70, v71
	ds_write_b64 v142, v[4:5] offset:15232
	s_waitcnt lgkmcnt(0)
	s_barrier
	s_waitcnt lgkmcnt(0)
	s_barrier
	s_waitcnt vmcnt(15)
	v_cvt_pk_f16_f32 v4, v72, v73
	v_cvt_pk_f16_f32 v5, v74, v75
	ds_write_b64 v143, v[4:5]
	s_waitcnt vmcnt(14)
	v_cvt_pk_f16_f32 v4, v104, v105
	v_cvt_pk_f16_f32 v5, v106, v107
	s_mov_b64 s[70:71], exec
	s_mov_b64 exec, s[78:79]
	ds_write_b64 v144, v[4:5]
	s_mov_b64 exec, s[70:71]
	s_waitcnt vmcnt(13)
	v_cvt_pk_f16_f32 v4, v76, v77
	v_cvt_pk_f16_f32 v5, v78, v79
	ds_write_b64 v143, v[4:5] offset:2176
	s_waitcnt vmcnt(12)
	v_cvt_pk_f16_f32 v4, v108, v109
	v_cvt_pk_f16_f32 v5, v110, v111
	s_mov_b64 s[70:71], exec
	s_mov_b64 exec, s[78:79]
	ds_write_b64 v144, v[4:5] offset:2176
	s_mov_b64 exec, s[70:71]
	s_waitcnt vmcnt(11)
	v_cvt_pk_f16_f32 v4, v80, v81
	v_cvt_pk_f16_f32 v5, v82, v83
	ds_write_b64 v143, v[4:5] offset:4352
	s_waitcnt vmcnt(10)
	v_cvt_pk_f16_f32 v4, v112, v113
	v_cvt_pk_f16_f32 v5, v114, v115
	s_mov_b64 s[70:71], exec
	s_mov_b64 exec, s[78:79]
	ds_write_b64 v144, v[4:5] offset:4352
	s_mov_b64 exec, s[70:71]
	s_waitcnt vmcnt(9)
	v_cvt_pk_f16_f32 v4, v84, v85
	v_cvt_pk_f16_f32 v5, v86, v87
	ds_write_b64 v143, v[4:5] offset:6528
	s_waitcnt vmcnt(8)
	v_cvt_pk_f16_f32 v4, v116, v117
	v_cvt_pk_f16_f32 v5, v118, v119
	s_mov_b64 s[70:71], exec
	s_mov_b64 exec, s[78:79]
	ds_write_b64 v144, v[4:5] offset:6528
	s_mov_b64 exec, s[70:71]
	s_waitcnt vmcnt(7)
	v_cvt_pk_f16_f32 v4, v88, v89
	v_cvt_pk_f16_f32 v5, v90, v91
	ds_write_b64 v143, v[4:5] offset:8704
	s_waitcnt vmcnt(6)
	v_cvt_pk_f16_f32 v4, v120, v121
	v_cvt_pk_f16_f32 v5, v122, v123
	s_mov_b64 s[70:71], exec
	s_mov_b64 exec, s[78:79]
	ds_write_b64 v144, v[4:5] offset:8704
	s_mov_b64 exec, s[70:71]
	s_waitcnt vmcnt(5)
	v_cvt_pk_f16_f32 v4, v92, v93
	v_cvt_pk_f16_f32 v5, v94, v95
	ds_write_b64 v143, v[4:5] offset:10880
	s_waitcnt vmcnt(4)
	v_cvt_pk_f16_f32 v4, v124, v125
	v_cvt_pk_f16_f32 v5, v126, v127
	s_mov_b64 s[70:71], exec
	s_mov_b64 exec, s[78:79]
	ds_write_b64 v144, v[4:5] offset:10880
	s_mov_b64 exec, s[70:71]
	s_waitcnt vmcnt(3)
	v_cvt_pk_f16_f32 v4, v96, v97
	v_cvt_pk_f16_f32 v5, v98, v99
	ds_write_b64 v143, v[4:5] offset:13056
	s_waitcnt vmcnt(2)
	v_cvt_pk_f16_f32 v4, v128, v129
	v_cvt_pk_f16_f32 v5, v130, v131
	s_mov_b64 s[70:71], exec
	s_mov_b64 exec, s[78:79]
	ds_write_b64 v144, v[4:5] offset:13056
	s_mov_b64 exec, s[70:71]
	s_waitcnt vmcnt(1)
	v_cvt_pk_f16_f32 v4, v100, v101
	v_cvt_pk_f16_f32 v5, v102, v103
	ds_write_b64 v143, v[4:5] offset:15232
	s_waitcnt vmcnt(0)
	v_cvt_pk_f16_f32 v4, v132, v133
	v_cvt_pk_f16_f32 v5, v134, v135
	s_mov_b64 s[70:71], exec
	s_mov_b64 exec, s[78:79]
	ds_write_b64 v144, v[4:5] offset:15232
	s_mov_b64 exec, s[70:71]
	s_waitcnt lgkmcnt(0)
	s_barrier
	s_waitcnt lgkmcnt(0)
	s_barrier
	s_barrier
	s_barrier
	s_endpgm
